# MoE expert-weight stream loads marked nt (read-once bytes)
# speedup vs baseline: 1.0405x; 1.0023x over previous
; #define LAS __attribute__((address_space(3)))
; #define MS_WLOAD(set, t) do { _Pragma("unroll") for (int r_ = 0; r_ < 4; ++r_) wr[set][r_] = __builtin_bit_cast(f32x4, __builtin_amdgcn_raw_buffer_load_b128(wrs, (int)wvo + r_ * LDW * 4, MS_CL(t) * (64 * LDW * 4), 0)); } while (0)
; #define MS_WCOMMIT(set, bufi) do { LAS unsigned char* wb_ = lds + (bufi) * MS_TILE; _Pragma("unroll") for (int i_ = 0; i_ < 4; ++i_) { \
;             u32x2 p_; p_.x = pk2(wr[set][0][i_], wr[set][1][i_]); p_.y = pk2(wr[set][2][i_], wr[set][3][i_]); \
;             *(LAS u32x2*)(wb_ + ((i_ < 2) ? lw0 : lw1) + i_ * 128) = p_; } } while (0)
; #define MS_XSLOAD(t) do { _Pragma("unroll") for (int i_ = 0; i_ < 6; ++i_) xs[i_] = __builtin_bit_cast(bf16x8, __builtin_amdgcn_raw_buffer_load_b128(xrs, (int)xso[i_], MS_CL(t) * 128, 0)); } while (0)
; #define MS_XSWRITE(bufi) do { _Pragma("unroll") for (int i_ = 0; i_ < 6; ++i_) *(LAS bf16x8*)(xw + (bufi) * MS_XBUF + i_ * 1024 + ((i_ & 1) ? (xwo ^ 64) : xwo)) = xs[i_]; } while (0)
;     ...
;         for (int rp = 0; rp < M; rp += 384) {
;             unsigned xso[6];
; #pragma unroll
;             for (int i = 0; i < 6; ++i) { int tok = rp + wave * 48 + 8 * i + (lane >> 3); tok = min(tok, M - 1); if (VAR == 5) tok &= 15; if (MODE == 0) tok = el[tok]; xso[i] = (unsigned)(tok * LDX * 2 + (lane & 7) * 16); }
;             LAS unsigned char* xw = lds + MS_XOFF + wave * MS_XWAVE; const int xwo = (lane >> 3) * 128 + (((lane & 7) ^ ((lane >> 4) & 3)) << 4);
;             const LAS unsigned char* xr = lds + MS_XOFF + wave * MS_XWAVE + tk * 128 + ((q ^ rd_g) << 4);
;             f32x4 acc[3][8];
; #pragma unroll
;             for (int mt = 0; mt < 3; ++mt)
; #pragma unroll
;                 for (int j = 0; j < 8; ++j) acc[mt][j] = (f32x4){0.f, 0.f, 0.f, 0.f};
;             f32x4 wr[2][4];
;             bf16x8 xs[6];
;     ...
;             const LAS unsigned char* xr1 = lds + MS_XOFF + wave * MS_XWAVE + tk * 128 + (((4 + q) ^ rd_g) << 4);
;             __syncthreads();
;             MS_XSLOAD(0); MS_WLOAD(0, 0); MS_WLOAD(1, 1);
;             MS_WCOMMIT(0, 0); MS_WLOAD(0, 2);
;             MS_XSWRITE(0); MS_XSLOAD(1);
;             __syncthreads();
.LBB0_1719:
	v_add_u32_e32 v4, s31, v162
	v_min_i32_e32 v2, s30, v4
	v_ashrrev_i32_e32 v3, 31, v2
	v_lshl_add_u64 v[2:3], v[2:3], 2, s[40:41]
	global_load_dword v182, v[2:3], off
	v_or_b32_e32 v2, 8, v4
	v_min_i32_e32 v2, s30, v2
	v_ashrrev_i32_e32 v3, 31, v2
	v_lshl_add_u64 v[2:3], v[2:3], 2, s[40:41]
	global_load_dword v183, v[2:3], off
	v_add_u32_e32 v2, 0x80, v4
	v_min_i32_e32 v2, s30, v2
	v_ashrrev_i32_e32 v3, 31, v2
	v_lshl_add_u64 v[2:3], v[2:3], 2, s[40:41]
	global_load_dword v184, v[2:3], off
	v_add_u32_e32 v2, 0x88, v4
	v_min_i32_e32 v2, s30, v2
	v_ashrrev_i32_e32 v3, 31, v2
	v_lshl_add_u64 v[2:3], v[2:3], 2, s[40:41]
	global_load_dword v185, v[2:3], off
	v_add_u32_e32 v2, 0x100, v4
	v_min_i32_e32 v2, s30, v2
	v_ashrrev_i32_e32 v3, 31, v2
	v_lshl_add_u64 v[2:3], v[2:3], 2, s[40:41]
	global_load_dword v186, v[2:3], off
	v_add_u32_e32 v2, 0x108, v4
	v_min_i32_e32 v2, s30, v2
	v_ashrrev_i32_e32 v3, 31, v2
	v_lshl_add_u64 v[2:3], v[2:3], 2, s[40:41]
	global_load_dword v187, v[2:3], off
	v_add_u32_e32 v188, 0, v161
	v_add_u32_e32 v189, s27, v172
	s_mov_b32 s0, -2
	s_barrier
	s_waitcnt vmcnt(0)
	v_lshl_or_b32 v182, v182, 12, v163
	v_lshl_or_b32 v183, v183, 12, v163
	v_lshl_or_b32 v184, v184, 12, v163
	v_lshl_or_b32 v185, v185, 12, v163
	v_lshl_or_b32 v186, v186, 12, v163
	v_lshl_or_b32 v187, v187, 12, v163
	buffer_load_dwordx4 v[2:5], v182, s[4:7], 0 offen
	buffer_load_dwordx4 v[6:9], v183, s[4:7], 0 offen
	buffer_load_dwordx4 v[10:13], v184, s[4:7], 0 offen
	buffer_load_dwordx4 v[14:17], v185, s[4:7], 0 offen
	buffer_load_dwordx4 v[18:21], v186, s[4:7], 0 offen
	buffer_load_dwordx4 v[22:25], v187, s[4:7], 0 offen
	buffer_load_dwordx4 v[26:29], v160, s[8:11], 0 offen nt
	buffer_load_dwordx4 v[30:33], v90, s[8:11], 0 offen nt
	buffer_load_dwordx4 v[34:37], v178, s[8:11], 0 offen nt
	buffer_load_dwordx4 v[38:41], v179, s[8:11], 0 offen nt
	buffer_load_dwordx4 v[74:77], v160, s[8:11], s11 offen nt
	buffer_load_dwordx4 v[78:81], v90, s[8:11], s11 offen nt
	buffer_load_dwordx4 v[82:85], v178, s[8:11], s11 offen nt
	buffer_load_dwordx4 v[86:89], v179, s[8:11], s11 offen nt
	s_waitcnt vmcnt(6)
	v_cvt_pk_bf16_f32 v42, v26, v30
	v_cvt_pk_bf16_f32 v26, v27, v31
	s_waitcnt vmcnt(4)
	v_cvt_pk_bf16_f32 v43, v34, v38
	v_cvt_pk_bf16_f32 v27, v35, v39
	ds_write2_b64 v188, v[42:43], v[26:27] offset1:16
	v_cvt_pk_bf16_f32 v26, v28, v32
	v_cvt_pk_bf16_f32 v27, v36, v40
	v_cvt_pk_bf16_f32 v28, v29, v33
	v_cvt_pk_bf16_f32 v29, v37, v41
	ds_write2_b64 v180, v[26:27], v[28:29] offset0:32 offset1:48
	buffer_load_dwordx4 v[96:99], v160, s[8:11], s22 offen nt
	buffer_load_dwordx4 v[100:103], v90, s[8:11], s22 offen nt
	buffer_load_dwordx4 v[104:107], v178, s[8:11], s22 offen nt
	buffer_load_dwordx4 v[108:111], v179, s[8:11], s22 offen nt
	ds_write_b128 v189, v[2:5] offset:32768
	ds_write_b128 v181, v[6:9] offset:33792
	ds_write_b128 v189, v[10:13] offset:34816
	ds_write_b128 v181, v[14:17] offset:35840
	ds_write_b128 v189, v[18:21] offset:36864
	ds_write_b128 v181, v[22:25] offset:37888
	buffer_load_dwordx4 v[132:135], v182, s[4:7], s92 offen
	buffer_load_dwordx4 v[124:127], v183, s[4:7], s92 offen
	buffer_load_dwordx4 v[140:143], v184, s[4:7], s92 offen
	buffer_load_dwordx4 v[144:147], v185, s[4:7], s92 offen
	buffer_load_dwordx4 v[128:131], v186, s[4:7], s92 offen
	buffer_load_dwordx4 v[136:139], v187, s[4:7], s92 offen
	v_mov_b32_e32 v2, 0
	v_mov_b32_e32 v3, v2
	v_mov_b32_e32 v4, v2
	v_mov_b32_e32 v5, v2
	v_mov_b32_e32 v10, v2
	v_mov_b32_e32 v11, v2
	v_mov_b32_e32 v12, v2
	v_mov_b32_e32 v13, v2
	v_mov_b32_e32 v18, v2
	v_mov_b32_e32 v19, v2
	v_mov_b32_e32 v20, v2
	v_mov_b32_e32 v21, v2
	v_mov_b32_e32 v26, v2
	v_mov_b32_e32 v27, v2
	v_mov_b32_e32 v28, v2
	v_mov_b32_e32 v29, v2
	v_mov_b32_e32 v6, v2
	v_mov_b32_e32 v7, v2
	v_mov_b32_e32 v8, v2
	v_mov_b32_e32 v9, v2
	v_mov_b32_e32 v14, v2
	v_mov_b32_e32 v15, v2
	v_mov_b32_e32 v16, v2
	v_mov_b32_e32 v17, v2
	v_mov_b32_e32 v22, v2
	v_mov_b32_e32 v23, v2
	v_mov_b32_e32 v24, v2
	v_mov_b32_e32 v25, v2
	v_mov_b32_e32 v30, v2
	v_mov_b32_e32 v31, v2
	v_mov_b32_e32 v32, v2
	v_mov_b32_e32 v33, v2
	v_mov_b32_e32 v34, v2
	v_mov_b32_e32 v35, v2
	v_mov_b32_e32 v36, v2
	v_mov_b32_e32 v37, v2
	v_mov_b32_e32 v42, v2
	v_mov_b32_e32 v43, v2
	v_mov_b32_e32 v44, v2
	v_mov_b32_e32 v45, v2
	v_mov_b32_e32 v50, v2
	v_mov_b32_e32 v51, v2
	v_mov_b32_e32 v52, v2
	v_mov_b32_e32 v53, v2
	v_mov_b32_e32 v58, v2
	v_mov_b32_e32 v59, v2
	v_mov_b32_e32 v60, v2
	v_mov_b32_e32 v61, v2
	v_mov_b32_e32 v38, v2
	v_mov_b32_e32 v39, v2
	v_mov_b32_e32 v40, v2
	v_mov_b32_e32 v41, v2
	v_mov_b32_e32 v46, v2
	v_mov_b32_e32 v47, v2
	v_mov_b32_e32 v48, v2
	v_mov_b32_e32 v49, v2
	v_mov_b32_e32 v54, v2
	v_mov_b32_e32 v55, v2
	v_mov_b32_e32 v56, v2
	v_mov_b32_e32 v57, v2
	v_mov_b32_e32 v62, v2
	v_mov_b32_e32 v63, v2
	v_mov_b32_e32 v64, v2
	v_mov_b32_e32 v65, v2
	v_mov_b32_e32 v66, v2
	v_mov_b32_e32 v67, v2
	v_mov_b32_e32 v68, v2
	v_mov_b32_e32 v69, v2
	v_mov_b32_e32 v92, v2
	v_mov_b32_e32 v93, v2
	v_mov_b32_e32 v94, v2
	v_mov_b32_e32 v95, v2
	v_mov_b32_e32 v116, v2
	v_mov_b32_e32 v117, v2
	v_mov_b32_e32 v118, v2
	v_mov_b32_e32 v119, v2
	v_mov_b32_e32 v148, v2
	v_mov_b32_e32 v149, v2
	v_mov_b32_e32 v150, v2
	v_mov_b32_e32 v151, v2
	v_mov_b32_e32 v70, v2
	v_mov_b32_e32 v71, v2
	v_mov_b32_e32 v72, v2
	v_mov_b32_e32 v73, v2
	v_mov_b32_e32 v112, v2
	v_mov_b32_e32 v113, v2
	v_mov_b32_e32 v114, v2
	v_mov_b32_e32 v115, v2
	v_mov_b32_e32 v120, v2
	v_mov_b32_e32 v121, v2
	v_mov_b32_e32 v122, v2
	v_mov_b32_e32 v123, v2
	v_mov_b32_e32 v152, v2
	v_mov_b32_e32 v153, v2
	v_mov_b32_e32 v154, v2
	v_mov_b32_e32 v155, v2
	s_waitcnt lgkmcnt(0)
	s_barrier
	s_sub_i32 s81, s28, s31
	s_add_i32 s82, s80, 0x100
	s_cmp_le_i32 s81, s82
	s_cbranch_scc1 .Lmoe_k_b
.LBB0_1720:
	s_add_i32 s0, s0, 2
	s_min_u32 s1, s0, 28
	s_lshl_b32 s12, s1, 17
	s_add_i32 s12, s12, 0x60000
	s_waitcnt vmcnt(12)
	v_cvt_pk_bf16_f32 v164, v74, v78
	s_waitcnt vmcnt(10)
	v_cvt_pk_bf16_f32 v165, v82, v86
	v_cvt_pk_bf16_f32 v166, v75, v79
	v_cvt_pk_bf16_f32 v167, v83, v87
	v_cvt_pk_bf16_f32 v190, v76, v80
	v_cvt_pk_bf16_f32 v191, v84, v88
	v_cvt_pk_bf16_f32 v192, v77, v81
	v_cvt_pk_bf16_f32 v193, v85, v89
	buffer_load_dwordx4 v[74:77], v160, s[8:11], s12 offen nt
	buffer_load_dwordx4 v[78:81], v90, s[8:11], s12 offen nt
	buffer_load_dwordx4 v[82:85], v178, s[8:11], s12 offen nt
	buffer_load_dwordx4 v[86:89], v179, s[8:11], s12 offen nt
	v_add_u32_e32 v194, 0x4000, v188
	v_add_u32_e32 v195, 0x4000, v180
	v_add_u32_e32 v214, v173, v174
	ds_write2_b64 v194, v[164:165], v[166:167] offset1:16
	ds_write2_b64 v195, v[190:191], v[192:193] offset0:32 offset1:48
	v_add_u32_e32 v215, v176, v174
	ds_read_b128 v[164:167], v214 offset:32768
	ds_read_b128 v[190:193], v214 offset:34816
	ds_read_b128 v[194:197], v214 offset:36864
	ds_read_b128 v[198:201], v215
	ds_read_b128 v[202:205], v215 offset:2048
	ds_read_b128 v[206:209], v215 offset:4096
	ds_read_b128 v[210:213], v215 offset:6144
	s_waitcnt lgkmcnt(3)
	v_mfma_f32_16x16x32_bf16 v[152:155], v[198:201], v[164:167], v[152:155]
	v_mfma_f32_16x16x32_bf16 v[62:65], v[198:201], v[190:193], v[62:65]
	v_mfma_f32_16x16x32_bf16 v[30:33], v[198:201], v[194:197], v[30:33]
	s_waitcnt lgkmcnt(2)
	v_mfma_f32_16x16x32_bf16 v[120:123], v[202:205], v[164:167], v[120:123]
	v_mfma_f32_16x16x32_bf16 v[54:57], v[202:205], v[190:193], v[54:57]
	v_mfma_f32_16x16x32_bf16 v[22:25], v[202:205], v[194:197], v[22:25]
	s_waitcnt lgkmcnt(1)
	v_mfma_f32_16x16x32_bf16 v[112:115], v[206:209], v[164:167], v[112:115]
	v_mfma_f32_16x16x32_bf16 v[46:49], v[206:209], v[190:193], v[46:49]
	v_mfma_f32_16x16x32_bf16 v[14:17], v[206:209], v[194:197], v[14:17]
	s_waitcnt lgkmcnt(0)
	v_mfma_f32_16x16x32_bf16 v[70:73], v[210:213], v[164:167], v[70:73]
	v_mfma_f32_16x16x32_bf16 v[38:41], v[210:213], v[190:193], v[38:41]
	v_mfma_f32_16x16x32_bf16 v[6:9], v[210:213], v[194:197], v[6:9]
	ds_read_b128 v[198:201], v215 offset:8192
	ds_read_b128 v[202:205], v215 offset:10240
	ds_read_b128 v[206:209], v215 offset:12288
	ds_read_b128 v[210:213], v215 offset:14336
	s_waitcnt lgkmcnt(3)
	v_mfma_f32_16x16x32_bf16 v[148:151], v[198:201], v[164:167], v[148:151]
	v_mfma_f32_16x16x32_bf16 v[58:61], v[198:201], v[190:193], v[58:61]
	v_mfma_f32_16x16x32_bf16 v[26:29], v[198:201], v[194:197], v[26:29]
	s_waitcnt lgkmcnt(2)
	v_mfma_f32_16x16x32_bf16 v[116:119], v[202:205], v[164:167], v[116:119]
	v_mfma_f32_16x16x32_bf16 v[50:53], v[202:205], v[190:193], v[50:53]
	v_mfma_f32_16x16x32_bf16 v[18:21], v[202:205], v[194:197], v[18:21]
	s_waitcnt lgkmcnt(1)
	v_mfma_f32_16x16x32_bf16 v[92:95], v[206:209], v[164:167], v[92:95]
	v_mfma_f32_16x16x32_bf16 v[42:45], v[206:209], v[190:193], v[42:45]
	v_mfma_f32_16x16x32_bf16 v[10:13], v[206:209], v[194:197], v[10:13]
	s_waitcnt lgkmcnt(0)
	v_mfma_f32_16x16x32_bf16 v[66:69], v[210:213], v[164:167], v[66:69]
	v_mfma_f32_16x16x32_bf16 v[34:37], v[210:213], v[190:193], v[34:37]
	v_mfma_f32_16x16x32_bf16 v[2:5], v[210:213], v[194:197], v[2:5]
	v_add_u32_e32 v216, v173, v175
	ds_read_b128 v[164:167], v216 offset:32768
	ds_read_b128 v[190:193], v216 offset:34816
	v_add_u32_e32 v217, v176, v175
	ds_read_b128 v[194:197], v216 offset:36864
	ds_read_b128 v[198:201], v217
	ds_read_b128 v[202:205], v217 offset:2048
	ds_read_b128 v[206:209], v217 offset:4096
	ds_read_b128 v[210:213], v217 offset:6144
	s_waitcnt lgkmcnt(3)
	v_mfma_f32_16x16x32_bf16 v[152:155], v[198:201], v[164:167], v[152:155]
	v_mfma_f32_16x16x32_bf16 v[62:65], v[198:201], v[190:193], v[62:65]
	v_mfma_f32_16x16x32_bf16 v[30:33], v[198:201], v[194:197], v[30:33]
	s_waitcnt lgkmcnt(2)
	v_mfma_f32_16x16x32_bf16 v[120:123], v[202:205], v[164:167], v[120:123]
	v_mfma_f32_16x16x32_bf16 v[54:57], v[202:205], v[190:193], v[54:57]
	v_mfma_f32_16x16x32_bf16 v[22:25], v[202:205], v[194:197], v[22:25]
	s_waitcnt lgkmcnt(1)
	v_mfma_f32_16x16x32_bf16 v[112:115], v[206:209], v[164:167], v[112:115]
	v_mfma_f32_16x16x32_bf16 v[46:49], v[206:209], v[190:193], v[46:49]
	v_mfma_f32_16x16x32_bf16 v[14:17], v[206:209], v[194:197], v[14:17]
	s_waitcnt lgkmcnt(0)
	v_mfma_f32_16x16x32_bf16 v[70:73], v[210:213], v[164:167], v[70:73]
	v_mfma_f32_16x16x32_bf16 v[38:41], v[210:213], v[190:193], v[38:41]
	v_mfma_f32_16x16x32_bf16 v[6:9], v[210:213], v[194:197], v[6:9]
	ds_read_b128 v[198:201], v217 offset:8192
	ds_read_b128 v[202:205], v217 offset:10240
	ds_read_b128 v[206:209], v217 offset:12288
	ds_read_b128 v[210:213], v217 offset:14336
	s_min_u32 s12, s0, 29
	s_lshl_b32 s12, s12, 7
	s_waitcnt vmcnt(9)
	ds_write_b128 v189, v[132:135] offset:38912
	s_waitcnt vmcnt(8)
	ds_write_b128 v181, v[124:127] offset:39936
	s_waitcnt vmcnt(7)
	ds_write_b128 v189, v[140:143] offset:40960
	s_waitcnt vmcnt(6)
	ds_write_b128 v181, v[144:147] offset:41984
	s_waitcnt vmcnt(5)
	ds_write_b128 v189, v[128:131] offset:43008
	s_waitcnt vmcnt(4)
	ds_write_b128 v181, v[136:139] offset:44032
	s_addk_i32 s12, 0x100
	s_waitcnt lgkmcnt(9)
	v_mfma_f32_16x16x32_bf16 v[148:151], v[198:201], v[164:167], v[148:151]
	buffer_load_dwordx4 v[124:127], v182, s[4:7], s12 offen
	buffer_load_dwordx4 v[128:131], v183, s[4:7], s12 offen
	buffer_load_dwordx4 v[132:135], v184, s[4:7], s12 offen
	buffer_load_dwordx4 v[136:139], v185, s[4:7], s12 offen
	buffer_load_dwordx4 v[140:143], v186, s[4:7], s12 offen
	buffer_load_dwordx4 v[144:147], v187, s[4:7], s12 offen
	s_min_u32 s12, s0, 27
	s_waitcnt lgkmcnt(0)
	v_mfma_f32_16x16x32_bf16 v[116:119], v[202:205], v[164:167], v[116:119]
	s_barrier
; #define LAS __attribute__((address_space(3)))
; #define MS_WLOAD(set, t) do { _Pragma("unroll") for (int r_ = 0; r_ < 4; ++r_) wr[set][r_] = __builtin_bit_cast(f32x4, __builtin_amdgcn_raw_buffer_load_b128(wrs, (int)wvo + r_ * LDW * 4, MS_CL(t) * (64 * LDW * 4), 0)); } while (0)
; #define MS_WCOMMIT(set, bufi) do { LAS unsigned char* wb_ = lds + (bufi) * MS_TILE; _Pragma("unroll") for (int i_ = 0; i_ < 4; ++i_) { \
;             u32x2 p_; p_.x = pk2(wr[set][0][i_], wr[set][1][i_]); p_.y = pk2(wr[set][2][i_], wr[set][3][i_]); \
;             *(LAS u32x2*)(wb_ + ((i_ < 2) ? lw0 : lw1) + i_ * 128) = p_; } } while (0)
; #define MS_XSLOAD(t) do { _Pragma("unroll") for (int i_ = 0; i_ < 6; ++i_) xs[i_] = __builtin_bit_cast(bf16x8, __builtin_amdgcn_raw_buffer_load_b128(xrs, (int)xso[i_], MS_CL(t) * 128, 0)); } while (0)
; #define MS_XSWRITE(bufi) do { _Pragma("unroll") for (int i_ = 0; i_ < 6; ++i_) *(LAS bf16x8*)(xw + (bufi) * MS_XBUF + i_ * 1024 + ((i_ & 1) ? (xwo ^ 64) : xwo)) = xs[i_]; } while (0)
; #define MS_STEP(I, J, t) do { MS_WCOMMIT(J, J); MS_WLOAD(J, (t) + 3); MS_COMPUTE(I); MS_XSWRITE(J); MS_XSLOAD((t) + 2); __syncthreads(); } while (0)
;     ...
;             const LAS unsigned char* xr1 = lds + MS_XOFF + wave * MS_XWAVE + tk * 128 + (((4 + q) ^ rd_g) << 4);
;             __syncthreads();
;             MS_XSLOAD(0); MS_WLOAD(0, 0); MS_WLOAD(1, 1);
;             MS_WCOMMIT(0, 0); MS_WLOAD(0, 2);
;             MS_XSWRITE(0); MS_XSLOAD(1);
;             __syncthreads();
; #pragma unroll 1
;             for (int t = 0; t < NT; t += 2) { MS_STEP(0, 1, t); MS_STEP(1, 0, t + 1); }
	s_lshl_b32 s12, s12, 17
	v_mfma_f32_16x16x32_bf16 v[92:95], v[206:209], v[164:167], v[92:95]
	s_add_i32 s12, s12, 0x80000
	v_mfma_f32_16x16x32_bf16 v[66:69], v[210:213], v[164:167], v[66:69]
	v_cvt_pk_bf16_f32 v164, v96, v100
	v_cvt_pk_bf16_f32 v165, v104, v108
	v_cvt_pk_bf16_f32 v96, v97, v101
	v_cvt_pk_bf16_f32 v97, v105, v109
	ds_write2_b64 v188, v[164:165], v[96:97] offset1:16
	v_cvt_pk_bf16_f32 v96, v98, v102
	v_cvt_pk_bf16_f32 v97, v106, v110
	v_cvt_pk_bf16_f32 v98, v99, v103
	v_cvt_pk_bf16_f32 v99, v107, v111
	ds_write2_b64 v180, v[96:97], v[98:99] offset0:32 offset1:48
	buffer_load_dwordx4 v[96:99], v160, s[8:11], s12 offen nt
	buffer_load_dwordx4 v[100:103], v90, s[8:11], s12 offen nt
	buffer_load_dwordx4 v[104:107], v178, s[8:11], s12 offen nt
	buffer_load_dwordx4 v[108:111], v179, s[8:11], s12 offen nt
	v_mfma_f32_16x16x32_bf16 v[58:61], v[198:201], v[190:193], v[58:61]
	v_mfma_f32_16x16x32_bf16 v[26:29], v[198:201], v[194:197], v[26:29]
	v_mfma_f32_16x16x32_bf16 v[50:53], v[202:205], v[190:193], v[50:53]
	v_mfma_f32_16x16x32_bf16 v[18:21], v[202:205], v[194:197], v[18:21]
	v_mfma_f32_16x16x32_bf16 v[42:45], v[206:209], v[190:193], v[42:45]
	v_mfma_f32_16x16x32_bf16 v[10:13], v[206:209], v[194:197], v[10:13]
	v_mfma_f32_16x16x32_bf16 v[34:37], v[210:213], v[190:193], v[34:37]
	v_mfma_f32_16x16x32_bf16 v[2:5], v[210:213], v[194:197], v[2:5]
	ds_read_b128 v[164:167], v214 offset:38912
	ds_read_b128 v[190:193], v214 offset:40960
	ds_read_b128 v[194:197], v214 offset:43008
	ds_read_b128 v[198:201], v215 offset:16384
	ds_read_b128 v[202:205], v215 offset:18432
	ds_read_b128 v[206:209], v215 offset:20480
	ds_read_b128 v[210:213], v215 offset:22528
	s_waitcnt lgkmcnt(3)
	v_mfma_f32_16x16x32_bf16 v[152:155], v[198:201], v[164:167], v[152:155]
	v_mfma_f32_16x16x32_bf16 v[62:65], v[198:201], v[190:193], v[62:65]
	v_mfma_f32_16x16x32_bf16 v[30:33], v[198:201], v[194:197], v[30:33]
	s_waitcnt lgkmcnt(2)
	v_mfma_f32_16x16x32_bf16 v[120:123], v[202:205], v[164:167], v[120:123]
	v_mfma_f32_16x16x32_bf16 v[54:57], v[202:205], v[190:193], v[54:57]
	v_mfma_f32_16x16x32_bf16 v[22:25], v[202:205], v[194:197], v[22:25]
	s_waitcnt lgkmcnt(1)
	v_mfma_f32_16x16x32_bf16 v[112:115], v[206:209], v[164:167], v[112:115]
	v_mfma_f32_16x16x32_bf16 v[46:49], v[206:209], v[190:193], v[46:49]
	v_mfma_f32_16x16x32_bf16 v[14:17], v[206:209], v[194:197], v[14:17]
	s_waitcnt lgkmcnt(0)
	v_mfma_f32_16x16x32_bf16 v[70:73], v[210:213], v[164:167], v[70:73]
	v_mfma_f32_16x16x32_bf16 v[38:41], v[210:213], v[190:193], v[38:41]
	v_mfma_f32_16x16x32_bf16 v[6:9], v[210:213], v[194:197], v[6:9]
	ds_read_b128 v[198:201], v215 offset:24576
	ds_read_b128 v[202:205], v215 offset:26624
	ds_read_b128 v[206:209], v215 offset:28672
	ds_read_b128 v[210:213], v215 offset:30720
	s_waitcnt lgkmcnt(3)
	v_mfma_f32_16x16x32_bf16 v[148:151], v[198:201], v[164:167], v[148:151]
	v_mfma_f32_16x16x32_bf16 v[58:61], v[198:201], v[190:193], v[58:61]
	v_mfma_f32_16x16x32_bf16 v[26:29], v[198:201], v[194:197], v[26:29]
	s_waitcnt lgkmcnt(2)
	v_mfma_f32_16x16x32_bf16 v[116:119], v[202:205], v[164:167], v[116:119]
	v_mfma_f32_16x16x32_bf16 v[50:53], v[202:205], v[190:193], v[50:53]
	v_mfma_f32_16x16x32_bf16 v[18:21], v[202:205], v[194:197], v[18:21]
	s_waitcnt lgkmcnt(1)
	v_mfma_f32_16x16x32_bf16 v[92:95], v[206:209], v[164:167], v[92:95]
	v_mfma_f32_16x16x32_bf16 v[42:45], v[206:209], v[190:193], v[42:45]
	v_mfma_f32_16x16x32_bf16 v[10:13], v[206:209], v[194:197], v[10:13]
	s_waitcnt lgkmcnt(0)
	v_mfma_f32_16x16x32_bf16 v[66:69], v[210:213], v[164:167], v[66:69]
	v_mfma_f32_16x16x32_bf16 v[34:37], v[210:213], v[190:193], v[34:37]
	v_mfma_f32_16x16x32_bf16 v[2:5], v[210:213], v[194:197], v[2:5]
	ds_read_b128 v[164:167], v216 offset:38912
	ds_read_b128 v[190:193], v216 offset:40960
	ds_read_b128 v[194:197], v216 offset:43008
	ds_read_b128 v[198:201], v217 offset:16384
	ds_read_b128 v[202:205], v217 offset:18432
	ds_read_b128 v[206:209], v217 offset:20480
	ds_read_b128 v[210:213], v217 offset:22528
	s_waitcnt lgkmcnt(3)
	v_mfma_f32_16x16x32_bf16 v[152:155], v[198:201], v[164:167], v[152:155]
	v_mfma_f32_16x16x32_bf16 v[62:65], v[198:201], v[190:193], v[62:65]
	v_mfma_f32_16x16x32_bf16 v[30:33], v[198:201], v[194:197], v[30:33]
	s_waitcnt lgkmcnt(2)
	v_mfma_f32_16x16x32_bf16 v[120:123], v[202:205], v[164:167], v[120:123]
	v_mfma_f32_16x16x32_bf16 v[54:57], v[202:205], v[190:193], v[54:57]
	v_mfma_f32_16x16x32_bf16 v[22:25], v[202:205], v[194:197], v[22:25]
	s_waitcnt lgkmcnt(1)
	v_mfma_f32_16x16x32_bf16 v[112:115], v[206:209], v[164:167], v[112:115]
	v_mfma_f32_16x16x32_bf16 v[46:49], v[206:209], v[190:193], v[46:49]
	v_mfma_f32_16x16x32_bf16 v[14:17], v[206:209], v[194:197], v[14:17]
	s_waitcnt lgkmcnt(0)
	v_mfma_f32_16x16x32_bf16 v[70:73], v[210:213], v[164:167], v[70:73]
	v_mfma_f32_16x16x32_bf16 v[38:41], v[210:213], v[190:193], v[38:41]
	v_mfma_f32_16x16x32_bf16 v[6:9], v[210:213], v[194:197], v[6:9]
	ds_read_b128 v[198:201], v217 offset:24576
	ds_read_b128 v[202:205], v217 offset:26624
	ds_read_b128 v[206:209], v217 offset:28672
	ds_read_b128 v[210:213], v217 offset:30720
	s_lshl_b32 s1, s1, 7
	s_waitcnt vmcnt(9)
	ds_write_b128 v189, v[124:127] offset:32768
	s_waitcnt vmcnt(8)
	ds_write_b128 v181, v[128:131] offset:33792
	s_waitcnt vmcnt(7)
	ds_write_b128 v189, v[132:135] offset:34816
	s_waitcnt vmcnt(6)
	ds_write_b128 v181, v[136:139] offset:35840
	s_waitcnt vmcnt(5)
	ds_write_b128 v189, v[140:143] offset:36864
	s_waitcnt vmcnt(4)
	ds_write_b128 v181, v[144:147] offset:37888
	s_addk_i32 s1, 0x180
	buffer_load_dwordx4 v[132:135], v182, s[4:7], s1 offen
	buffer_load_dwordx4 v[124:127], v183, s[4:7], s1 offen
	buffer_load_dwordx4 v[140:143], v184, s[4:7], s1 offen
	buffer_load_dwordx4 v[144:147], v185, s[4:7], s1 offen
	buffer_load_dwordx4 v[128:131], v186, s[4:7], s1 offen
	buffer_load_dwordx4 v[136:139], v187, s[4:7], s1 offen
	s_waitcnt lgkmcnt(9)
	v_mfma_f32_16x16x32_bf16 v[148:151], v[198:201], v[164:167], v[148:151]
	s_cmp_gt_u32 s0, 29
	s_waitcnt lgkmcnt(0)
	s_barrier
	v_mfma_f32_16x16x32_bf16 v[58:61], v[198:201], v[190:193], v[58:61]
	v_mfma_f32_16x16x32_bf16 v[26:29], v[198:201], v[194:197], v[26:29]
	v_mfma_f32_16x16x32_bf16 v[116:119], v[202:205], v[164:167], v[116:119]
	v_mfma_f32_16x16x32_bf16 v[50:53], v[202:205], v[190:193], v[50:53]
	v_mfma_f32_16x16x32_bf16 v[18:21], v[202:205], v[194:197], v[18:21]
	v_mfma_f32_16x16x32_bf16 v[92:95], v[206:209], v[164:167], v[92:95]
	v_mfma_f32_16x16x32_bf16 v[42:45], v[206:209], v[190:193], v[42:45]
	v_mfma_f32_16x16x32_bf16 v[10:13], v[206:209], v[194:197], v[10:13]
	v_mfma_f32_16x16x32_bf16 v[66:69], v[210:213], v[164:167], v[66:69]
	v_mfma_f32_16x16x32_bf16 v[34:37], v[210:213], v[190:193], v[34:37]
	v_mfma_f32_16x16x32_bf16 v[2:5], v[210:213], v[194:197], v[2:5]
	s_cbranch_scc0 .LBB0_1720
	s_branch .Lmoe_k_done
; #define LAS __attribute__((address_space(3)))
; #define MS_WLOAD(set, t) do { _Pragma("unroll") for (int r_ = 0; r_ < 4; ++r_) wr[set][r_] = __builtin_bit_cast(f32x4, __builtin_amdgcn_raw_buffer_load_b128(wrs, (int)wvo + r_ * LDW * 4, MS_CL(t) * (64 * LDW * 4), 0)); } while (0)
; #define MS_WCOMMIT(set, bufi) do { LAS unsigned char* wb_ = lds + (bufi) * MS_TILE; _Pragma("unroll") for (int i_ = 0; i_ < 4; ++i_) { \
;             u32x2 p_; p_.x = pk2(wr[set][0][i_], wr[set][1][i_]); p_.y = pk2(wr[set][2][i_], wr[set][3][i_]); \
;             *(LAS u32x2*)(wb_ + ((i_ < 2) ? lw0 : lw1) + i_ * 128) = p_; } } while (0)
; #define MS_XSLOAD(t) do { _Pragma("unroll") for (int i_ = 0; i_ < 6; ++i_) xs[i_] = __builtin_bit_cast(bf16x8, __builtin_amdgcn_raw_buffer_load_b128(xrs, (int)xso[i_], MS_CL(t) * 128, 0)); } while (0)
; #define MS_XSWRITE(bufi) do { _Pragma("unroll") for (int i_ = 0; i_ < 6; ++i_) *(LAS bf16x8*)(xw + (bufi) * MS_XBUF + i_ * 1024 + ((i_ & 1) ? (xwo ^ 64) : xwo)) = xs[i_]; } while (0)
; #define MS_STEP(I, J, t) do { MS_WCOMMIT(J, J); MS_WLOAD(J, (t) + 3); MS_COMPUTE(I); MS_XSWRITE(J); MS_XSLOAD((t) + 2); __syncthreads(); } while (0)
;     ...
;             const LAS unsigned char* xr1 = lds + MS_XOFF + wave * MS_XWAVE + tk * 128 + (((4 + q) ^ rd_g) << 4);
;             __syncthreads();
;             MS_XSLOAD(0); MS_WLOAD(0, 0); MS_WLOAD(1, 1);
;             MS_WCOMMIT(0, 0); MS_WLOAD(0, 2);
;             MS_XSWRITE(0); MS_XSLOAD(1);
;             __syncthreads();
; #pragma unroll 1
;             for (int t = 0; t < NT; t += 2) { MS_STEP(0, 1, t); MS_STEP(1, 0, t + 1); }
.Lmoe_k_b:
	s_add_i32 s0, s0, 2
	s_min_u32 s1, s0, 28
	s_lshl_b32 s12, s1, 17
	s_add_i32 s12, s12, 0x60000
	s_waitcnt vmcnt(12)
	v_cvt_pk_bf16_f32 v164, v74, v78
	s_waitcnt vmcnt(10)
	v_cvt_pk_bf16_f32 v165, v82, v86
	v_cvt_pk_bf16_f32 v166, v75, v79
	v_cvt_pk_bf16_f32 v167, v83, v87
	v_cvt_pk_bf16_f32 v190, v76, v80
	v_cvt_pk_bf16_f32 v191, v84, v88
	v_cvt_pk_bf16_f32 v192, v77, v81
	v_cvt_pk_bf16_f32 v193, v85, v89
	buffer_load_dwordx4 v[74:77], v160, s[8:11], s12 offen nt
	buffer_load_dwordx4 v[78:81], v90, s[8:11], s12 offen nt
	buffer_load_dwordx4 v[82:85], v178, s[8:11], s12 offen nt
	buffer_load_dwordx4 v[86:89], v179, s[8:11], s12 offen nt
	v_add_u32_e32 v194, 0x4000, v188
	v_add_u32_e32 v195, 0x4000, v180
	v_add_u32_e32 v214, v173, v174
	ds_write2_b64 v194, v[164:165], v[166:167] offset1:16
	ds_write2_b64 v195, v[190:191], v[192:193] offset0:32 offset1:48
	v_add_u32_e32 v215, v176, v174
	ds_read_b128 v[164:167], v214 offset:32768
	ds_read_b128 v[190:193], v214 offset:34816
	ds_read_b128 v[198:201], v215
	ds_read_b128 v[202:205], v215 offset:2048
	ds_read_b128 v[206:209], v215 offset:4096
	ds_read_b128 v[210:213], v215 offset:6144
	s_waitcnt lgkmcnt(3)
	v_mfma_f32_16x16x32_bf16 v[152:155], v[198:201], v[164:167], v[152:155]
	v_mfma_f32_16x16x32_bf16 v[62:65], v[198:201], v[190:193], v[62:65]
	s_waitcnt lgkmcnt(2)
	v_mfma_f32_16x16x32_bf16 v[120:123], v[202:205], v[164:167], v[120:123]
	v_mfma_f32_16x16x32_bf16 v[54:57], v[202:205], v[190:193], v[54:57]
	s_waitcnt lgkmcnt(1)
	v_mfma_f32_16x16x32_bf16 v[112:115], v[206:209], v[164:167], v[112:115]
	v_mfma_f32_16x16x32_bf16 v[46:49], v[206:209], v[190:193], v[46:49]
	s_waitcnt lgkmcnt(0)
	v_mfma_f32_16x16x32_bf16 v[70:73], v[210:213], v[164:167], v[70:73]
	v_mfma_f32_16x16x32_bf16 v[38:41], v[210:213], v[190:193], v[38:41]
	ds_read_b128 v[198:201], v215 offset:8192
	ds_read_b128 v[202:205], v215 offset:10240
	ds_read_b128 v[206:209], v215 offset:12288
	ds_read_b128 v[210:213], v215 offset:14336
	s_waitcnt lgkmcnt(3)
	v_mfma_f32_16x16x32_bf16 v[148:151], v[198:201], v[164:167], v[148:151]
	v_mfma_f32_16x16x32_bf16 v[58:61], v[198:201], v[190:193], v[58:61]
	s_waitcnt lgkmcnt(2)
	v_mfma_f32_16x16x32_bf16 v[116:119], v[202:205], v[164:167], v[116:119]
	v_mfma_f32_16x16x32_bf16 v[50:53], v[202:205], v[190:193], v[50:53]
	s_waitcnt lgkmcnt(1)
	v_mfma_f32_16x16x32_bf16 v[92:95], v[206:209], v[164:167], v[92:95]
	v_mfma_f32_16x16x32_bf16 v[42:45], v[206:209], v[190:193], v[42:45]
	s_waitcnt lgkmcnt(0)
	v_mfma_f32_16x16x32_bf16 v[66:69], v[210:213], v[164:167], v[66:69]
	v_mfma_f32_16x16x32_bf16 v[34:37], v[210:213], v[190:193], v[34:37]
	v_add_u32_e32 v216, v173, v175
	ds_read_b128 v[164:167], v216 offset:32768
	ds_read_b128 v[190:193], v216 offset:34816
	v_add_u32_e32 v217, v176, v175
	ds_read_b128 v[198:201], v217
	ds_read_b128 v[202:205], v217 offset:2048
	ds_read_b128 v[206:209], v217 offset:4096
	ds_read_b128 v[210:213], v217 offset:6144
	s_waitcnt lgkmcnt(3)
	v_mfma_f32_16x16x32_bf16 v[152:155], v[198:201], v[164:167], v[152:155]
	v_mfma_f32_16x16x32_bf16 v[62:65], v[198:201], v[190:193], v[62:65]
	s_waitcnt lgkmcnt(2)
	v_mfma_f32_16x16x32_bf16 v[120:123], v[202:205], v[164:167], v[120:123]
	v_mfma_f32_16x16x32_bf16 v[54:57], v[202:205], v[190:193], v[54:57]
	s_waitcnt lgkmcnt(1)
	v_mfma_f32_16x16x32_bf16 v[112:115], v[206:209], v[164:167], v[112:115]
	v_mfma_f32_16x16x32_bf16 v[46:49], v[206:209], v[190:193], v[46:49]
	s_waitcnt lgkmcnt(0)
	v_mfma_f32_16x16x32_bf16 v[70:73], v[210:213], v[164:167], v[70:73]
	v_mfma_f32_16x16x32_bf16 v[38:41], v[210:213], v[190:193], v[38:41]
	ds_read_b128 v[198:201], v217 offset:8192
	ds_read_b128 v[202:205], v217 offset:10240
	ds_read_b128 v[206:209], v217 offset:12288
	ds_read_b128 v[210:213], v217 offset:14336
	s_min_u32 s12, s0, 29
	s_lshl_b32 s12, s12, 7
	s_waitcnt vmcnt(7)
	ds_write_b128 v189, v[132:135] offset:38912
	s_waitcnt vmcnt(6)
	ds_write_b128 v181, v[124:127] offset:39936
	s_waitcnt vmcnt(5)
	ds_write_b128 v189, v[140:143] offset:40960
	s_waitcnt vmcnt(4)
	ds_write_b128 v181, v[144:147] offset:41984
	s_addk_i32 s12, 0x100
	s_waitcnt lgkmcnt(7)
	v_mfma_f32_16x16x32_bf16 v[148:151], v[198:201], v[164:167], v[148:151]
	buffer_load_dwordx4 v[124:127], v182, s[4:7], s12 offen
	buffer_load_dwordx4 v[128:131], v183, s[4:7], s12 offen
	buffer_load_dwordx4 v[132:135], v184, s[4:7], s12 offen
	buffer_load_dwordx4 v[136:139], v185, s[4:7], s12 offen
	s_min_u32 s12, s0, 27
	s_waitcnt lgkmcnt(0)
	v_mfma_f32_16x16x32_bf16 v[116:119], v[202:205], v[164:167], v[116:119]
	s_barrier
; #define LAS __attribute__((address_space(3)))
; #define MS_WLOAD(set, t) do { _Pragma("unroll") for (int r_ = 0; r_ < 4; ++r_) wr[set][r_] = __builtin_bit_cast(f32x4, __builtin_amdgcn_raw_buffer_load_b128(wrs, (int)wvo + r_ * LDW * 4, MS_CL(t) * (64 * LDW * 4), 0)); } while (0)
; #define MS_WCOMMIT(set, bufi) do { LAS unsigned char* wb_ = lds + (bufi) * MS_TILE; _Pragma("unroll") for (int i_ = 0; i_ < 4; ++i_) { \
;             u32x2 p_; p_.x = pk2(wr[set][0][i_], wr[set][1][i_]); p_.y = pk2(wr[set][2][i_], wr[set][3][i_]); \
;             *(LAS u32x2*)(wb_ + ((i_ < 2) ? lw0 : lw1) + i_ * 128) = p_; } } while (0)
; #define MS_XSLOAD(t) do { _Pragma("unroll") for (int i_ = 0; i_ < 6; ++i_) xs[i_] = __builtin_bit_cast(bf16x8, __builtin_amdgcn_raw_buffer_load_b128(xrs, (int)xso[i_], MS_CL(t) * 128, 0)); } while (0)
; #define MS_XSWRITE(bufi) do { _Pragma("unroll") for (int i_ = 0; i_ < 6; ++i_) *(LAS bf16x8*)(xw + (bufi) * MS_XBUF + i_ * 1024 + ((i_ & 1) ? (xwo ^ 64) : xwo)) = xs[i_]; } while (0)
; #define MS_STEP(I, J, t) do { MS_WCOMMIT(J, J); MS_WLOAD(J, (t) + 3); MS_COMPUTE(I); MS_XSWRITE(J); MS_XSLOAD((t) + 2); __syncthreads(); } while (0)
;     ...
;             const LAS unsigned char* xr1 = lds + MS_XOFF + wave * MS_XWAVE + tk * 128 + (((4 + q) ^ rd_g) << 4);
;             __syncthreads();
;             MS_XSLOAD(0); MS_WLOAD(0, 0); MS_WLOAD(1, 1);
;             MS_WCOMMIT(0, 0); MS_WLOAD(0, 2);
;             MS_XSWRITE(0); MS_XSLOAD(1);
;             __syncthreads();
; #pragma unroll 1
;             for (int t = 0; t < NT; t += 2) { MS_STEP(0, 1, t); MS_STEP(1, 0, t + 1); }
	s_lshl_b32 s12, s12, 17
	v_mfma_f32_16x16x32_bf16 v[92:95], v[206:209], v[164:167], v[92:95]
	s_add_i32 s12, s12, 0x80000
	v_mfma_f32_16x16x32_bf16 v[66:69], v[210:213], v[164:167], v[66:69]
	v_cvt_pk_bf16_f32 v164, v96, v100
	v_cvt_pk_bf16_f32 v165, v104, v108
	v_cvt_pk_bf16_f32 v96, v97, v101
	v_cvt_pk_bf16_f32 v97, v105, v109
	ds_write2_b64 v188, v[164:165], v[96:97] offset1:16
	v_cvt_pk_bf16_f32 v96, v98, v102
	v_cvt_pk_bf16_f32 v97, v106, v110
	v_cvt_pk_bf16_f32 v98, v99, v103
	v_cvt_pk_bf16_f32 v99, v107, v111
	ds_write2_b64 v180, v[96:97], v[98:99] offset0:32 offset1:48
	buffer_load_dwordx4 v[96:99], v160, s[8:11], s12 offen nt
	buffer_load_dwordx4 v[100:103], v90, s[8:11], s12 offen nt
	buffer_load_dwordx4 v[104:107], v178, s[8:11], s12 offen nt
	buffer_load_dwordx4 v[108:111], v179, s[8:11], s12 offen nt
	v_mfma_f32_16x16x32_bf16 v[58:61], v[198:201], v[190:193], v[58:61]
	v_mfma_f32_16x16x32_bf16 v[50:53], v[202:205], v[190:193], v[50:53]
	v_mfma_f32_16x16x32_bf16 v[42:45], v[206:209], v[190:193], v[42:45]
	v_mfma_f32_16x16x32_bf16 v[34:37], v[210:213], v[190:193], v[34:37]
	ds_read_b128 v[164:167], v214 offset:38912
	ds_read_b128 v[190:193], v214 offset:40960
	ds_read_b128 v[198:201], v215 offset:16384
	ds_read_b128 v[202:205], v215 offset:18432
	ds_read_b128 v[206:209], v215 offset:20480
	ds_read_b128 v[210:213], v215 offset:22528
	s_waitcnt lgkmcnt(3)
	v_mfma_f32_16x16x32_bf16 v[152:155], v[198:201], v[164:167], v[152:155]
	v_mfma_f32_16x16x32_bf16 v[62:65], v[198:201], v[190:193], v[62:65]
	s_waitcnt lgkmcnt(2)
	v_mfma_f32_16x16x32_bf16 v[120:123], v[202:205], v[164:167], v[120:123]
	v_mfma_f32_16x16x32_bf16 v[54:57], v[202:205], v[190:193], v[54:57]
	s_waitcnt lgkmcnt(1)
	v_mfma_f32_16x16x32_bf16 v[112:115], v[206:209], v[164:167], v[112:115]
	v_mfma_f32_16x16x32_bf16 v[46:49], v[206:209], v[190:193], v[46:49]
	s_waitcnt lgkmcnt(0)
	v_mfma_f32_16x16x32_bf16 v[70:73], v[210:213], v[164:167], v[70:73]
	v_mfma_f32_16x16x32_bf16 v[38:41], v[210:213], v[190:193], v[38:41]
	ds_read_b128 v[198:201], v215 offset:24576
	ds_read_b128 v[202:205], v215 offset:26624
	ds_read_b128 v[206:209], v215 offset:28672
	ds_read_b128 v[210:213], v215 offset:30720
	s_waitcnt lgkmcnt(3)
	v_mfma_f32_16x16x32_bf16 v[148:151], v[198:201], v[164:167], v[148:151]
	v_mfma_f32_16x16x32_bf16 v[58:61], v[198:201], v[190:193], v[58:61]
	s_waitcnt lgkmcnt(2)
	v_mfma_f32_16x16x32_bf16 v[116:119], v[202:205], v[164:167], v[116:119]
	v_mfma_f32_16x16x32_bf16 v[50:53], v[202:205], v[190:193], v[50:53]
	s_waitcnt lgkmcnt(1)
	v_mfma_f32_16x16x32_bf16 v[92:95], v[206:209], v[164:167], v[92:95]
	v_mfma_f32_16x16x32_bf16 v[42:45], v[206:209], v[190:193], v[42:45]
	s_waitcnt lgkmcnt(0)
	v_mfma_f32_16x16x32_bf16 v[66:69], v[210:213], v[164:167], v[66:69]
	v_mfma_f32_16x16x32_bf16 v[34:37], v[210:213], v[190:193], v[34:37]
	ds_read_b128 v[164:167], v216 offset:38912
	ds_read_b128 v[190:193], v216 offset:40960
	ds_read_b128 v[198:201], v217 offset:16384
	ds_read_b128 v[202:205], v217 offset:18432
	ds_read_b128 v[206:209], v217 offset:20480
	ds_read_b128 v[210:213], v217 offset:22528
	s_waitcnt lgkmcnt(3)
	v_mfma_f32_16x16x32_bf16 v[152:155], v[198:201], v[164:167], v[152:155]
	v_mfma_f32_16x16x32_bf16 v[62:65], v[198:201], v[190:193], v[62:65]
	s_waitcnt lgkmcnt(2)
	v_mfma_f32_16x16x32_bf16 v[120:123], v[202:205], v[164:167], v[120:123]
	v_mfma_f32_16x16x32_bf16 v[54:57], v[202:205], v[190:193], v[54:57]
	s_waitcnt lgkmcnt(1)
	v_mfma_f32_16x16x32_bf16 v[112:115], v[206:209], v[164:167], v[112:115]
	v_mfma_f32_16x16x32_bf16 v[46:49], v[206:209], v[190:193], v[46:49]
	s_waitcnt lgkmcnt(0)
	v_mfma_f32_16x16x32_bf16 v[70:73], v[210:213], v[164:167], v[70:73]
	v_mfma_f32_16x16x32_bf16 v[38:41], v[210:213], v[190:193], v[38:41]
	ds_read_b128 v[198:201], v217 offset:24576
	ds_read_b128 v[202:205], v217 offset:26624
	ds_read_b128 v[206:209], v217 offset:28672
	ds_read_b128 v[210:213], v217 offset:30720
	s_lshl_b32 s1, s1, 7
	s_waitcnt vmcnt(7)
	ds_write_b128 v189, v[124:127] offset:32768
	s_waitcnt vmcnt(6)
	ds_write_b128 v181, v[128:131] offset:33792
	s_waitcnt vmcnt(5)
	ds_write_b128 v189, v[132:135] offset:34816
	s_waitcnt vmcnt(4)
	ds_write_b128 v181, v[136:139] offset:35840
	s_addk_i32 s1, 0x180
	buffer_load_dwordx4 v[132:135], v182, s[4:7], s1 offen
	buffer_load_dwordx4 v[124:127], v183, s[4:7], s1 offen
	buffer_load_dwordx4 v[140:143], v184, s[4:7], s1 offen
	buffer_load_dwordx4 v[144:147], v185, s[4:7], s1 offen
	s_waitcnt lgkmcnt(7)
	v_mfma_f32_16x16x32_bf16 v[148:151], v[198:201], v[164:167], v[148:151]
	s_cmp_gt_u32 s0, 29
	s_waitcnt lgkmcnt(0)
	s_barrier
	v_mfma_f32_16x16x32_bf16 v[58:61], v[198:201], v[190:193], v[58:61]
	v_mfma_f32_16x16x32_bf16 v[116:119], v[202:205], v[164:167], v[116:119]
	v_mfma_f32_16x16x32_bf16 v[50:53], v[202:205], v[190:193], v[50:53]
	v_mfma_f32_16x16x32_bf16 v[92:95], v[206:209], v[164:167], v[92:95]
	v_mfma_f32_16x16x32_bf16 v[42:45], v[206:209], v[190:193], v[42:45]
	v_mfma_f32_16x16x32_bf16 v[66:69], v[210:213], v[164:167], v[66:69]
	v_mfma_f32_16x16x32_bf16 v[34:37], v[210:213], v[190:193], v[34:37]
	s_cbranch_scc0 .Lmoe_k_b

; #define LAS __attribute__((address_space(3)))
; #define MS_WLOAD(set, t) do { _Pragma("unroll") for (int r_ = 0; r_ < 4; ++r_) wr[set][r_] = __builtin_bit_cast(f32x4, __builtin_amdgcn_raw_buffer_load_b128(wrs, (int)wvo + r_ * LDW * 4, MS_CL(t) * (64 * LDW * 4), 0)); } while (0)
; #define MS_WCOMMIT(set, bufi) do { LAS unsigned char* wb_ = lds + (bufi) * MS_TILE; _Pragma("unroll") for (int i_ = 0; i_ < 4; ++i_) { \
;             u32x2 p_; p_.x = pk2(wr[set][0][i_], wr[set][1][i_]); p_.y = pk2(wr[set][2][i_], wr[set][3][i_]); \
;             *(LAS u32x2*)(wb_ + ((i_ < 2) ? lw0 : lw1) + i_ * 128) = p_; } } while (0)
; #define MS_XSLOAD(t) do { _Pragma("unroll") for (int i_ = 0; i_ < 6; ++i_) xs[i_] = __builtin_bit_cast(bf16x8, __builtin_amdgcn_raw_buffer_load_b128(xrs, (int)xso[i_], MS_CL(t) * 128, 0)); } while (0)
; #define MS_XSWRITE(bufi) do { _Pragma("unroll") for (int i_ = 0; i_ < 6; ++i_) *(LAS bf16x8*)(xw + (bufi) * MS_XBUF + i_ * 1024 + ((i_ & 1) ? (xwo ^ 64) : xwo)) = xs[i_]; } while (0)
;     ...
;         for (int rp = 0; rp < M; rp += 384) {
;             unsigned xso[6];
; #pragma unroll
;             for (int i = 0; i < 6; ++i) { int tok = rp + wave * 48 + 8 * i + (lane >> 3); tok = min(tok, M - 1); if (VAR == 5) tok &= 15; if (MODE == 0) tok = el[tok]; xso[i] = (unsigned)(tok * LDX * 2 + (lane & 7) * 16); }
;             LAS unsigned char* xw = lds + MS_XOFF + wave * MS_XWAVE; const int xwo = (lane >> 3) * 128 + (((lane & 7) ^ ((lane >> 4) & 3)) << 4);
;             const LAS unsigned char* xr = lds + MS_XOFF + wave * MS_XWAVE + tk * 128 + ((q ^ rd_g) << 4);
;             f32x4 acc[3][8];
; #pragma unroll
;             for (int mt = 0; mt < 3; ++mt)
; #pragma unroll
;                 for (int j = 0; j < 8; ++j) acc[mt][j] = (f32x4){0.f, 0.f, 0.f, 0.f};
;             f32x4 wr[2][4];
;             bf16x8 xs[6];
;     ...
;             const LAS unsigned char* xr1 = lds + MS_XOFF + wave * MS_XWAVE + tk * 128 + (((4 + q) ^ rd_g) << 4);
;             __syncthreads();
;             MS_XSLOAD(0); MS_WLOAD(0, 0); MS_WLOAD(1, 1);
;             MS_WCOMMIT(0, 0); MS_WLOAD(0, 2);
;             MS_XSWRITE(0); MS_XSLOAD(1);
;             __syncthreads();
.LBB0_1784:
	v_add_u32_e32 v2, s31, v162
	v_min_i32_e32 v3, s25, v2
	v_lshl_or_b32 v182, v3, 10, v163
	v_or_b32_e32 v3, 8, v2
	v_min_i32_e32 v3, s25, v3
	v_lshl_or_b32 v183, v3, 10, v163
	v_add_u32_e32 v3, 0x80, v2
	v_min_i32_e32 v3, s25, v3
	v_lshl_or_b32 v184, v3, 10, v163
	v_add_u32_e32 v3, 0x88, v2
	v_min_i32_e32 v3, s25, v3
	v_lshl_or_b32 v185, v3, 10, v163
	v_add_u32_e32 v3, 0x100, v2
	v_add_u32_e32 v2, 0x108, v2
	v_min_i32_e32 v3, s25, v3
	v_min_i32_e32 v2, s25, v2
	s_barrier
	buffer_load_dwordx4 v[52:55], v160, s[8:11], 0 offen nt
	buffer_load_dwordx4 v[56:59], v90, s[8:11], 0 offen nt
	buffer_load_dwordx4 v[60:63], v178, s[8:11], 0 offen nt
	buffer_load_dwordx4 v[64:67], v179, s[8:11], 0 offen nt
	v_lshl_or_b32 v186, v3, 10, v163
	v_lshl_or_b32 v187, v2, 10, v163
	buffer_load_dwordx4 v[68:71], v182, s[4:7], 0 offen
	buffer_load_dwordx4 v[72:75], v183, s[4:7], 0 offen
	buffer_load_dwordx4 v[76:79], v184, s[4:7], 0 offen
	buffer_load_dwordx4 v[80:83], v185, s[4:7], 0 offen
	buffer_load_dwordx4 v[84:87], v186, s[4:7], 0 offen
	buffer_load_dwordx4 v[96:99], v187, s[4:7], 0 offen
	buffer_load_dwordx4 v[2:5], v160, s[8:11], s23 offen nt
	buffer_load_dwordx4 v[6:9], v178, s[8:11], s23 offen nt
	buffer_load_dwordx4 v[18:21], v160, s[8:11], s93 offen nt
	buffer_load_dwordx4 v[10:13], v90, s[8:11], s23 offen nt
	buffer_load_dwordx4 v[22:25], v90, s[8:11], s93 offen nt
	buffer_load_dwordx4 v[26:29], v178, s[8:11], s93 offen nt
	buffer_load_dwordx4 v[14:17], v179, s[8:11], s23 offen nt
	buffer_load_dwordx4 v[30:33], v179, s[8:11], s93 offen nt
	buffer_load_dwordx4 v[104:107], v182, s[4:7], s92 offen
	buffer_load_dwordx4 v[92:95], v183, s[4:7], s92 offen
	buffer_load_dwordx4 v[112:115], v184, s[4:7], s92 offen
	buffer_load_dwordx4 v[116:119], v185, s[4:7], s92 offen
	buffer_load_dwordx4 v[100:103], v186, s[4:7], s92 offen
	buffer_load_dwordx4 v[108:111], v187, s[4:7], s92 offen
	v_add_u32_e32 v188, 0, v161
	v_mov_b32_e32 v34, 0
	v_add_u32_e32 v189, s29, v172
	s_mov_b32 s2, -2
	v_mov_b32_e32 v35, v34
	v_mov_b32_e32 v36, v34
	v_mov_b32_e32 v37, v34
	v_mov_b32_e32 v38, v34
	v_mov_b32_e32 v39, v34
	v_mov_b32_e32 v40, v34
	v_mov_b32_e32 v41, v34
	v_mov_b32_e32 v42, v34
	v_mov_b32_e32 v43, v34
	v_mov_b32_e32 v44, v34
	v_mov_b32_e32 v45, v34
	v_mov_b32_e32 v46, v34
	v_mov_b32_e32 v47, v34
	v_mov_b32_e32 v48, v34
	v_mov_b32_e32 v49, v34
	v_mov_b32_e32 v50, v34
	v_mov_b32_e32 v51, v34
	v_mov_b32_e32 v120, v34
	v_mov_b32_e32 v121, v34
	v_mov_b32_e32 v122, v34
	v_mov_b32_e32 v123, v34
	v_mov_b32_e32 v124, v34
	v_mov_b32_e32 v125, v34
	v_mov_b32_e32 v126, v34
	v_mov_b32_e32 v127, v34
	v_mov_b32_e32 v128, v34
	v_mov_b32_e32 v129, v34
	v_mov_b32_e32 v130, v34
	v_mov_b32_e32 v131, v34
	v_mov_b32_e32 v132, v34
	v_mov_b32_e32 v133, v34
	v_mov_b32_e32 v134, v34
	v_mov_b32_e32 v135, v34
	v_mov_b32_e32 v136, v34
	v_mov_b32_e32 v137, v34
	v_mov_b32_e32 v138, v34
	v_mov_b32_e32 v139, v34
	v_mov_b32_e32 v140, v34
	v_mov_b32_e32 v141, v34
	v_mov_b32_e32 v142, v34
	v_mov_b32_e32 v143, v34
	v_mov_b32_e32 v144, v34
	v_mov_b32_e32 v145, v34
	v_mov_b32_e32 v146, v34
	v_mov_b32_e32 v147, v34
	v_mov_b32_e32 v148, v34
	v_mov_b32_e32 v149, v34
	v_mov_b32_e32 v150, v34
	v_mov_b32_e32 v151, v34
	v_mov_b32_e32 v152, v34
	v_mov_b32_e32 v153, v34
	v_mov_b32_e32 v154, v34
	v_mov_b32_e32 v155, v34
	s_waitcnt vmcnt(22)
	v_cvt_pk_bf16_f32 v88, v52, v56
	v_cvt_pk_bf16_f32 v52, v53, v57
	s_waitcnt vmcnt(20)
	v_cvt_pk_bf16_f32 v89, v60, v64
	v_cvt_pk_bf16_f32 v53, v61, v65
	v_cvt_pk_bf16_f32 v56, v54, v58
	v_cvt_pk_bf16_f32 v57, v62, v66
	v_cvt_pk_bf16_f32 v54, v55, v59
	v_cvt_pk_bf16_f32 v55, v63, v67
	ds_write2_b64 v188, v[88:89], v[52:53] offset1:16
	ds_write2_b64 v180, v[56:57], v[54:55] offset0:32 offset1:48
	s_waitcnt vmcnt(19)
	ds_write_b128 v189, v[68:71] offset:32768
	s_waitcnt vmcnt(18)
	ds_write_b128 v181, v[72:75] offset:33792
	s_waitcnt vmcnt(17)
	ds_write_b128 v189, v[76:79] offset:34816
	s_waitcnt vmcnt(16)
	ds_write_b128 v181, v[80:83] offset:35840
	s_waitcnt vmcnt(15)
	ds_write_b128 v189, v[84:87] offset:36864
	s_waitcnt vmcnt(14)
	ds_write_b128 v181, v[96:99] offset:37888
	v_mov_b32_e32 v52, v34
	v_mov_b32_e32 v53, v34
	v_mov_b32_e32 v54, v34
	v_mov_b32_e32 v55, v34
	v_mov_b32_e32 v56, v34
	v_mov_b32_e32 v57, v34
	v_mov_b32_e32 v58, v34
	v_mov_b32_e32 v59, v34
	v_mov_b32_e32 v60, v34
	v_mov_b32_e32 v61, v34
	v_mov_b32_e32 v62, v34
	v_mov_b32_e32 v63, v34
	v_mov_b32_e32 v64, v34
	v_mov_b32_e32 v65, v34
	v_mov_b32_e32 v66, v34
	v_mov_b32_e32 v67, v34
	v_mov_b32_e32 v68, v34
	v_mov_b32_e32 v69, v34
	v_mov_b32_e32 v70, v34
	v_mov_b32_e32 v71, v34
	v_mov_b32_e32 v72, v34
	v_mov_b32_e32 v73, v34
	v_mov_b32_e32 v74, v34
	v_mov_b32_e32 v75, v34
	v_mov_b32_e32 v76, v34
	v_mov_b32_e32 v77, v34
	v_mov_b32_e32 v78, v34
	v_mov_b32_e32 v79, v34
	v_mov_b32_e32 v80, v34
	v_mov_b32_e32 v81, v34
	v_mov_b32_e32 v82, v34
	v_mov_b32_e32 v83, v34
	v_mov_b32_e32 v84, v34
	v_mov_b32_e32 v85, v34
	v_mov_b32_e32 v86, v34
	v_mov_b32_e32 v87, v34
	v_mov_b32_e32 v88, v34
	v_mov_b32_e32 v89, v34
	v_mov_b32_e32 v96, v34
	v_mov_b32_e32 v97, v34
	v_mov_b32_e32 v98, v34
	v_mov_b32_e32 v99, v34
	s_waitcnt lgkmcnt(0)
	s_barrier
	s_sub_i32 s81, s30, s31
	s_add_i32 s82, s80, 0x100
	s_cmp_le_i32 s81, s82
	s_cbranch_scc1 .Lmoe_l_b
.LBB0_1785:
	s_add_i32 s2, s2, 2
	s_min_u32 s3, s2, 4
	s_lshl_b32 s33, s3, 19
	s_add_i32 s33, s33, 0x180000
	s_waitcnt vmcnt(10)
	v_cvt_pk_bf16_f32 v164, v2, v10
	s_waitcnt vmcnt(7)
	v_cvt_pk_bf16_f32 v165, v6, v14
	v_cvt_pk_bf16_f32 v166, v3, v11
	v_cvt_pk_bf16_f32 v167, v7, v15
	v_cvt_pk_bf16_f32 v190, v4, v12
	v_cvt_pk_bf16_f32 v191, v8, v16
	v_cvt_pk_bf16_f32 v192, v5, v13
	v_cvt_pk_bf16_f32 v193, v9, v17
	buffer_load_dwordx4 v[2:5], v160, s[8:11], s33 offen nt
	buffer_load_dwordx4 v[10:13], v90, s[8:11], s33 offen nt
	buffer_load_dwordx4 v[6:9], v178, s[8:11], s33 offen nt
	buffer_load_dwordx4 v[14:17], v179, s[8:11], s33 offen nt
	v_add_u32_e32 v194, 0x4000, v188
	v_add_u32_e32 v195, 0x4000, v180
	v_add_u32_e32 v214, v173, v174
	ds_write2_b64 v194, v[164:165], v[166:167] offset1:16
	ds_write2_b64 v195, v[190:191], v[192:193] offset0:32 offset1:48
	v_add_u32_e32 v215, v176, v174
	ds_read_b128 v[164:167], v214 offset:32768
	ds_read_b128 v[190:193], v214 offset:34816
	ds_read_b128 v[194:197], v214 offset:36864
	ds_read_b128 v[198:201], v215
	ds_read_b128 v[202:205], v215 offset:2048
	ds_read_b128 v[206:209], v215 offset:4096
	ds_read_b128 v[210:213], v215 offset:6144
	s_waitcnt lgkmcnt(3)
	v_mfma_f32_16x16x32_bf16 v[152:155], v[198:201], v[164:167], v[152:155]
	v_mfma_f32_16x16x32_bf16 v[120:123], v[198:201], v[190:193], v[120:123]
	v_mfma_f32_16x16x32_bf16 v[62:65], v[198:201], v[194:197], v[62:65]
	s_waitcnt lgkmcnt(2)
	v_mfma_f32_16x16x32_bf16 v[148:151], v[202:205], v[164:167], v[148:151]
	v_mfma_f32_16x16x32_bf16 v[96:99], v[202:205], v[190:193], v[96:99]
	v_mfma_f32_16x16x32_bf16 v[58:61], v[202:205], v[194:197], v[58:61]
	s_waitcnt lgkmcnt(1)
	v_mfma_f32_16x16x32_bf16 v[144:147], v[206:209], v[164:167], v[144:147]
	v_mfma_f32_16x16x32_bf16 v[86:89], v[206:209], v[190:193], v[86:89]
	v_mfma_f32_16x16x32_bf16 v[54:57], v[206:209], v[194:197], v[54:57]
	s_waitcnt lgkmcnt(0)
	v_mfma_f32_16x16x32_bf16 v[140:143], v[210:213], v[164:167], v[140:143]
	v_mfma_f32_16x16x32_bf16 v[82:85], v[210:213], v[190:193], v[82:85]
	v_mfma_f32_16x16x32_bf16 v[50:53], v[210:213], v[194:197], v[50:53]
	ds_read_b128 v[198:201], v215 offset:8192
	ds_read_b128 v[202:205], v215 offset:10240
	ds_read_b128 v[206:209], v215 offset:12288
	ds_read_b128 v[210:213], v215 offset:14336
	s_waitcnt lgkmcnt(3)
	v_mfma_f32_16x16x32_bf16 v[136:139], v[198:201], v[164:167], v[136:139]
	v_mfma_f32_16x16x32_bf16 v[78:81], v[198:201], v[190:193], v[78:81]
	v_mfma_f32_16x16x32_bf16 v[46:49], v[198:201], v[194:197], v[46:49]
	s_waitcnt lgkmcnt(2)
	v_mfma_f32_16x16x32_bf16 v[132:135], v[202:205], v[164:167], v[132:135]
	v_mfma_f32_16x16x32_bf16 v[74:77], v[202:205], v[190:193], v[74:77]
	v_mfma_f32_16x16x32_bf16 v[42:45], v[202:205], v[194:197], v[42:45]
	s_waitcnt lgkmcnt(1)
	v_mfma_f32_16x16x32_bf16 v[128:131], v[206:209], v[164:167], v[128:131]
	v_mfma_f32_16x16x32_bf16 v[70:73], v[206:209], v[190:193], v[70:73]
	v_mfma_f32_16x16x32_bf16 v[38:41], v[206:209], v[194:197], v[38:41]
	s_waitcnt lgkmcnt(0)
	v_mfma_f32_16x16x32_bf16 v[124:127], v[210:213], v[164:167], v[124:127]
	v_mfma_f32_16x16x32_bf16 v[66:69], v[210:213], v[190:193], v[66:69]
	v_mfma_f32_16x16x32_bf16 v[34:37], v[210:213], v[194:197], v[34:37]
	v_add_u32_e32 v216, v173, v175
	ds_read_b128 v[164:167], v216 offset:32768
	ds_read_b128 v[190:193], v216 offset:34816
	v_add_u32_e32 v217, v176, v175
	ds_read_b128 v[194:197], v216 offset:36864
	ds_read_b128 v[198:201], v217
	ds_read_b128 v[202:205], v217 offset:2048
	ds_read_b128 v[206:209], v217 offset:4096
	ds_read_b128 v[210:213], v217 offset:6144
	s_waitcnt lgkmcnt(3)
	v_mfma_f32_16x16x32_bf16 v[152:155], v[198:201], v[164:167], v[152:155]
	v_mfma_f32_16x16x32_bf16 v[120:123], v[198:201], v[190:193], v[120:123]
	v_mfma_f32_16x16x32_bf16 v[62:65], v[198:201], v[194:197], v[62:65]
	s_waitcnt lgkmcnt(2)
	v_mfma_f32_16x16x32_bf16 v[148:151], v[202:205], v[164:167], v[148:151]
	v_mfma_f32_16x16x32_bf16 v[96:99], v[202:205], v[190:193], v[96:99]
	v_mfma_f32_16x16x32_bf16 v[58:61], v[202:205], v[194:197], v[58:61]
	s_waitcnt lgkmcnt(1)
	v_mfma_f32_16x16x32_bf16 v[144:147], v[206:209], v[164:167], v[144:147]
	v_mfma_f32_16x16x32_bf16 v[86:89], v[206:209], v[190:193], v[86:89]
	v_mfma_f32_16x16x32_bf16 v[54:57], v[206:209], v[194:197], v[54:57]
	s_waitcnt lgkmcnt(0)
	v_mfma_f32_16x16x32_bf16 v[140:143], v[210:213], v[164:167], v[140:143]
	v_mfma_f32_16x16x32_bf16 v[82:85], v[210:213], v[190:193], v[82:85]
	v_mfma_f32_16x16x32_bf16 v[50:53], v[210:213], v[194:197], v[50:53]
	ds_read_b128 v[198:201], v217 offset:8192
	ds_read_b128 v[202:205], v217 offset:10240
	ds_read_b128 v[206:209], v217 offset:12288
	ds_read_b128 v[210:213], v217 offset:14336
	s_min_u32 s33, s2, 5
	s_lshl_b32 s33, s33, 7
	s_waitcnt vmcnt(9)
	ds_write_b128 v189, v[104:107] offset:38912
	s_waitcnt vmcnt(8)
	ds_write_b128 v181, v[92:95] offset:39936
	s_waitcnt vmcnt(7)
	ds_write_b128 v189, v[112:115] offset:40960
	s_waitcnt vmcnt(6)
	ds_write_b128 v181, v[116:119] offset:41984
	s_waitcnt vmcnt(5)
	ds_write_b128 v189, v[100:103] offset:43008
	s_waitcnt vmcnt(4)
	ds_write_b128 v181, v[108:111] offset:44032
	s_addk_i32 s33, 0x100
	s_waitcnt lgkmcnt(9)
	v_mfma_f32_16x16x32_bf16 v[136:139], v[198:201], v[164:167], v[136:139]
	buffer_load_dwordx4 v[92:95], v182, s[4:7], s33 offen
	buffer_load_dwordx4 v[100:103], v183, s[4:7], s33 offen
	buffer_load_dwordx4 v[104:107], v184, s[4:7], s33 offen
	buffer_load_dwordx4 v[108:111], v185, s[4:7], s33 offen
	buffer_load_dwordx4 v[112:115], v186, s[4:7], s33 offen
	buffer_load_dwordx4 v[116:119], v187, s[4:7], s33 offen
	s_min_u32 s33, s2, 3
	s_waitcnt lgkmcnt(0)
	v_mfma_f32_16x16x32_bf16 v[132:135], v[202:205], v[164:167], v[132:135]
	s_barrier
; #define LAS __attribute__((address_space(3)))
; #define MS_WLOAD(set, t) do { _Pragma("unroll") for (int r_ = 0; r_ < 4; ++r_) wr[set][r_] = __builtin_bit_cast(f32x4, __builtin_amdgcn_raw_buffer_load_b128(wrs, (int)wvo + r_ * LDW * 4, MS_CL(t) * (64 * LDW * 4), 0)); } while (0)
; #define MS_WCOMMIT(set, bufi) do { LAS unsigned char* wb_ = lds + (bufi) * MS_TILE; _Pragma("unroll") for (int i_ = 0; i_ < 4; ++i_) { \
;             u32x2 p_; p_.x = pk2(wr[set][0][i_], wr[set][1][i_]); p_.y = pk2(wr[set][2][i_], wr[set][3][i_]); \
;             *(LAS u32x2*)(wb_ + ((i_ < 2) ? lw0 : lw1) + i_ * 128) = p_; } } while (0)
; #define MS_XSLOAD(t) do { _Pragma("unroll") for (int i_ = 0; i_ < 6; ++i_) xs[i_] = __builtin_bit_cast(bf16x8, __builtin_amdgcn_raw_buffer_load_b128(xrs, (int)xso[i_], MS_CL(t) * 128, 0)); } while (0)
; #define MS_XSWRITE(bufi) do { _Pragma("unroll") for (int i_ = 0; i_ < 6; ++i_) *(LAS bf16x8*)(xw + (bufi) * MS_XBUF + i_ * 1024 + ((i_ & 1) ? (xwo ^ 64) : xwo)) = xs[i_]; } while (0)
; #define MS_STEP(I, J, t) do { MS_WCOMMIT(J, J); MS_WLOAD(J, (t) + 3); MS_COMPUTE(I); MS_XSWRITE(J); MS_XSLOAD((t) + 2); __syncthreads(); } while (0)
;     ...
;             const LAS unsigned char* xr1 = lds + MS_XOFF + wave * MS_XWAVE + tk * 128 + (((4 + q) ^ rd_g) << 4);
;             __syncthreads();
;             MS_XSLOAD(0); MS_WLOAD(0, 0); MS_WLOAD(1, 1);
;             MS_WCOMMIT(0, 0); MS_WLOAD(0, 2);
;             MS_XSWRITE(0); MS_XSLOAD(1);
;             __syncthreads();
; #pragma unroll 1
;             for (int t = 0; t < NT; t += 2) { MS_STEP(0, 1, t); MS_STEP(1, 0, t + 1); }
	s_lshl_b32 s33, s33, 19
	v_mfma_f32_16x16x32_bf16 v[128:131], v[206:209], v[164:167], v[128:131]
	s_bitset1_b32 s33, 21
	v_mfma_f32_16x16x32_bf16 v[124:127], v[210:213], v[164:167], v[124:127]
	v_cvt_pk_bf16_f32 v164, v18, v22
	v_cvt_pk_bf16_f32 v165, v26, v30
	v_cvt_pk_bf16_f32 v18, v19, v23
	v_cvt_pk_bf16_f32 v19, v27, v31
	ds_write2_b64 v188, v[164:165], v[18:19] offset1:16
	v_cvt_pk_bf16_f32 v18, v20, v24
	v_cvt_pk_bf16_f32 v19, v28, v32
	v_cvt_pk_bf16_f32 v20, v21, v25
	v_cvt_pk_bf16_f32 v21, v29, v33
	ds_write2_b64 v180, v[18:19], v[20:21] offset0:32 offset1:48
	buffer_load_dwordx4 v[18:21], v160, s[8:11], s33 offen nt
	buffer_load_dwordx4 v[22:25], v90, s[8:11], s33 offen nt
	buffer_load_dwordx4 v[26:29], v178, s[8:11], s33 offen nt
	buffer_load_dwordx4 v[30:33], v179, s[8:11], s33 offen nt
	v_mfma_f32_16x16x32_bf16 v[78:81], v[198:201], v[190:193], v[78:81]
	v_mfma_f32_16x16x32_bf16 v[46:49], v[198:201], v[194:197], v[46:49]
	v_mfma_f32_16x16x32_bf16 v[74:77], v[202:205], v[190:193], v[74:77]
	v_mfma_f32_16x16x32_bf16 v[42:45], v[202:205], v[194:197], v[42:45]
	v_mfma_f32_16x16x32_bf16 v[70:73], v[206:209], v[190:193], v[70:73]
	v_mfma_f32_16x16x32_bf16 v[38:41], v[206:209], v[194:197], v[38:41]
	v_mfma_f32_16x16x32_bf16 v[66:69], v[210:213], v[190:193], v[66:69]
	v_mfma_f32_16x16x32_bf16 v[34:37], v[210:213], v[194:197], v[34:37]
	ds_read_b128 v[164:167], v214 offset:38912
	ds_read_b128 v[190:193], v214 offset:40960
	ds_read_b128 v[194:197], v214 offset:43008
	ds_read_b128 v[198:201], v215 offset:16384
	ds_read_b128 v[202:205], v215 offset:18432
	ds_read_b128 v[206:209], v215 offset:20480
	ds_read_b128 v[210:213], v215 offset:22528
	s_waitcnt lgkmcnt(3)
	v_mfma_f32_16x16x32_bf16 v[152:155], v[198:201], v[164:167], v[152:155]
	v_mfma_f32_16x16x32_bf16 v[120:123], v[198:201], v[190:193], v[120:123]
	v_mfma_f32_16x16x32_bf16 v[62:65], v[198:201], v[194:197], v[62:65]
	s_waitcnt lgkmcnt(2)
	v_mfma_f32_16x16x32_bf16 v[148:151], v[202:205], v[164:167], v[148:151]
	v_mfma_f32_16x16x32_bf16 v[96:99], v[202:205], v[190:193], v[96:99]
	v_mfma_f32_16x16x32_bf16 v[58:61], v[202:205], v[194:197], v[58:61]
	s_waitcnt lgkmcnt(1)
	v_mfma_f32_16x16x32_bf16 v[144:147], v[206:209], v[164:167], v[144:147]
	v_mfma_f32_16x16x32_bf16 v[86:89], v[206:209], v[190:193], v[86:89]
	v_mfma_f32_16x16x32_bf16 v[54:57], v[206:209], v[194:197], v[54:57]
	s_waitcnt lgkmcnt(0)
	v_mfma_f32_16x16x32_bf16 v[140:143], v[210:213], v[164:167], v[140:143]
	v_mfma_f32_16x16x32_bf16 v[82:85], v[210:213], v[190:193], v[82:85]
	v_mfma_f32_16x16x32_bf16 v[50:53], v[210:213], v[194:197], v[50:53]
	ds_read_b128 v[198:201], v215 offset:24576
	ds_read_b128 v[202:205], v215 offset:26624
	ds_read_b128 v[206:209], v215 offset:28672
	ds_read_b128 v[210:213], v215 offset:30720
	s_waitcnt lgkmcnt(3)
	v_mfma_f32_16x16x32_bf16 v[136:139], v[198:201], v[164:167], v[136:139]
	v_mfma_f32_16x16x32_bf16 v[78:81], v[198:201], v[190:193], v[78:81]
	v_mfma_f32_16x16x32_bf16 v[46:49], v[198:201], v[194:197], v[46:49]
	s_waitcnt lgkmcnt(2)
	v_mfma_f32_16x16x32_bf16 v[132:135], v[202:205], v[164:167], v[132:135]
	v_mfma_f32_16x16x32_bf16 v[74:77], v[202:205], v[190:193], v[74:77]
	v_mfma_f32_16x16x32_bf16 v[42:45], v[202:205], v[194:197], v[42:45]
	s_waitcnt lgkmcnt(1)
	v_mfma_f32_16x16x32_bf16 v[128:131], v[206:209], v[164:167], v[128:131]
	v_mfma_f32_16x16x32_bf16 v[70:73], v[206:209], v[190:193], v[70:73]
	v_mfma_f32_16x16x32_bf16 v[38:41], v[206:209], v[194:197], v[38:41]
	s_waitcnt lgkmcnt(0)
	v_mfma_f32_16x16x32_bf16 v[124:127], v[210:213], v[164:167], v[124:127]
	v_mfma_f32_16x16x32_bf16 v[66:69], v[210:213], v[190:193], v[66:69]
	v_mfma_f32_16x16x32_bf16 v[34:37], v[210:213], v[194:197], v[34:37]
	ds_read_b128 v[164:167], v216 offset:38912
	ds_read_b128 v[190:193], v216 offset:40960
	ds_read_b128 v[194:197], v216 offset:43008
	ds_read_b128 v[198:201], v217 offset:16384
	ds_read_b128 v[202:205], v217 offset:18432
	ds_read_b128 v[206:209], v217 offset:20480
	ds_read_b128 v[210:213], v217 offset:22528
	s_waitcnt lgkmcnt(3)
	v_mfma_f32_16x16x32_bf16 v[152:155], v[198:201], v[164:167], v[152:155]
	v_mfma_f32_16x16x32_bf16 v[120:123], v[198:201], v[190:193], v[120:123]
	v_mfma_f32_16x16x32_bf16 v[62:65], v[198:201], v[194:197], v[62:65]
	s_waitcnt lgkmcnt(2)
	v_mfma_f32_16x16x32_bf16 v[148:151], v[202:205], v[164:167], v[148:151]
	v_mfma_f32_16x16x32_bf16 v[96:99], v[202:205], v[190:193], v[96:99]
	v_mfma_f32_16x16x32_bf16 v[58:61], v[202:205], v[194:197], v[58:61]
	s_waitcnt lgkmcnt(1)
	v_mfma_f32_16x16x32_bf16 v[144:147], v[206:209], v[164:167], v[144:147]
	v_mfma_f32_16x16x32_bf16 v[86:89], v[206:209], v[190:193], v[86:89]
	v_mfma_f32_16x16x32_bf16 v[54:57], v[206:209], v[194:197], v[54:57]
	s_waitcnt lgkmcnt(0)
	v_mfma_f32_16x16x32_bf16 v[140:143], v[210:213], v[164:167], v[140:143]
	v_mfma_f32_16x16x32_bf16 v[82:85], v[210:213], v[190:193], v[82:85]
	v_mfma_f32_16x16x32_bf16 v[50:53], v[210:213], v[194:197], v[50:53]
	ds_read_b128 v[198:201], v217 offset:24576
	ds_read_b128 v[202:205], v217 offset:26624
	ds_read_b128 v[206:209], v217 offset:28672
	ds_read_b128 v[210:213], v217 offset:30720
	s_lshl_b32 s3, s3, 7
	s_waitcnt vmcnt(9)
	ds_write_b128 v189, v[92:95] offset:32768
	s_waitcnt vmcnt(8)
	ds_write_b128 v181, v[100:103] offset:33792
	s_waitcnt vmcnt(7)
	ds_write_b128 v189, v[104:107] offset:34816
	s_waitcnt vmcnt(6)
	ds_write_b128 v181, v[108:111] offset:35840
	s_waitcnt vmcnt(5)
	ds_write_b128 v189, v[112:115] offset:36864
	s_waitcnt vmcnt(4)
	ds_write_b128 v181, v[116:119] offset:37888
	s_addk_i32 s3, 0x180
	buffer_load_dwordx4 v[104:107], v182, s[4:7], s3 offen
	buffer_load_dwordx4 v[92:95], v183, s[4:7], s3 offen
	buffer_load_dwordx4 v[112:115], v184, s[4:7], s3 offen
	buffer_load_dwordx4 v[116:119], v185, s[4:7], s3 offen
	buffer_load_dwordx4 v[100:103], v186, s[4:7], s3 offen
	buffer_load_dwordx4 v[108:111], v187, s[4:7], s3 offen
	s_waitcnt lgkmcnt(9)
	v_mfma_f32_16x16x32_bf16 v[136:139], v[198:201], v[164:167], v[136:139]
	s_cmp_gt_u32 s2, 5
	s_waitcnt lgkmcnt(0)
	s_barrier
	v_mfma_f32_16x16x32_bf16 v[78:81], v[198:201], v[190:193], v[78:81]
	v_mfma_f32_16x16x32_bf16 v[46:49], v[198:201], v[194:197], v[46:49]
	v_mfma_f32_16x16x32_bf16 v[132:135], v[202:205], v[164:167], v[132:135]
	v_mfma_f32_16x16x32_bf16 v[74:77], v[202:205], v[190:193], v[74:77]
	v_mfma_f32_16x16x32_bf16 v[42:45], v[202:205], v[194:197], v[42:45]
	v_mfma_f32_16x16x32_bf16 v[128:131], v[206:209], v[164:167], v[128:131]
	v_mfma_f32_16x16x32_bf16 v[70:73], v[206:209], v[190:193], v[70:73]
	v_mfma_f32_16x16x32_bf16 v[38:41], v[206:209], v[194:197], v[38:41]
	v_mfma_f32_16x16x32_bf16 v[124:127], v[210:213], v[164:167], v[124:127]
	v_mfma_f32_16x16x32_bf16 v[66:69], v[210:213], v[190:193], v[66:69]
	v_mfma_f32_16x16x32_bf16 v[34:37], v[210:213], v[194:197], v[34:37]
	s_cbranch_scc0 .LBB0_1785
	s_branch .Lmoe_l_done
; #define LAS __attribute__((address_space(3)))
; #define MS_WLOAD(set, t) do { _Pragma("unroll") for (int r_ = 0; r_ < 4; ++r_) wr[set][r_] = __builtin_bit_cast(f32x4, __builtin_amdgcn_raw_buffer_load_b128(wrs, (int)wvo + r_ * LDW * 4, MS_CL(t) * (64 * LDW * 4), 0)); } while (0)
; #define MS_WCOMMIT(set, bufi) do { LAS unsigned char* wb_ = lds + (bufi) * MS_TILE; _Pragma("unroll") for (int i_ = 0; i_ < 4; ++i_) { \
;             u32x2 p_; p_.x = pk2(wr[set][0][i_], wr[set][1][i_]); p_.y = pk2(wr[set][2][i_], wr[set][3][i_]); \
;             *(LAS u32x2*)(wb_ + ((i_ < 2) ? lw0 : lw1) + i_ * 128) = p_; } } while (0)
; #define MS_XSLOAD(t) do { _Pragma("unroll") for (int i_ = 0; i_ < 6; ++i_) xs[i_] = __builtin_bit_cast(bf16x8, __builtin_amdgcn_raw_buffer_load_b128(xrs, (int)xso[i_], MS_CL(t) * 128, 0)); } while (0)
; #define MS_XSWRITE(bufi) do { _Pragma("unroll") for (int i_ = 0; i_ < 6; ++i_) *(LAS bf16x8*)(xw + (bufi) * MS_XBUF + i_ * 1024 + ((i_ & 1) ? (xwo ^ 64) : xwo)) = xs[i_]; } while (0)
; #define MS_STEP(I, J, t) do { MS_WCOMMIT(J, J); MS_WLOAD(J, (t) + 3); MS_COMPUTE(I); MS_XSWRITE(J); MS_XSLOAD((t) + 2); __syncthreads(); } while (0)
;     ...
;             const LAS unsigned char* xr1 = lds + MS_XOFF + wave * MS_XWAVE + tk * 128 + (((4 + q) ^ rd_g) << 4);
;             __syncthreads();
;             MS_XSLOAD(0); MS_WLOAD(0, 0); MS_WLOAD(1, 1);
;             MS_WCOMMIT(0, 0); MS_WLOAD(0, 2);
;             MS_XSWRITE(0); MS_XSLOAD(1);
;             __syncthreads();
; #pragma unroll 1
;             for (int t = 0; t < NT; t += 2) { MS_STEP(0, 1, t); MS_STEP(1, 0, t + 1); }
.Lmoe_l_b:
	s_add_i32 s2, s2, 2
	s_min_u32 s3, s2, 4
	s_lshl_b32 s33, s3, 19
	s_add_i32 s33, s33, 0x180000
	s_waitcnt vmcnt(10)
	v_cvt_pk_bf16_f32 v164, v2, v10
	s_waitcnt vmcnt(7)
	v_cvt_pk_bf16_f32 v165, v6, v14
	v_cvt_pk_bf16_f32 v166, v3, v11
	v_cvt_pk_bf16_f32 v167, v7, v15
	v_cvt_pk_bf16_f32 v190, v4, v12
	v_cvt_pk_bf16_f32 v191, v8, v16
	v_cvt_pk_bf16_f32 v192, v5, v13
	v_cvt_pk_bf16_f32 v193, v9, v17
	buffer_load_dwordx4 v[2:5], v160, s[8:11], s33 offen nt
	buffer_load_dwordx4 v[10:13], v90, s[8:11], s33 offen nt
	buffer_load_dwordx4 v[6:9], v178, s[8:11], s33 offen nt
	buffer_load_dwordx4 v[14:17], v179, s[8:11], s33 offen nt
	v_add_u32_e32 v194, 0x4000, v188
	v_add_u32_e32 v195, 0x4000, v180
	v_add_u32_e32 v214, v173, v174
	ds_write2_b64 v194, v[164:165], v[166:167] offset1:16
	ds_write2_b64 v195, v[190:191], v[192:193] offset0:32 offset1:48
	v_add_u32_e32 v215, v176, v174
	ds_read_b128 v[164:167], v214 offset:32768
	ds_read_b128 v[190:193], v214 offset:34816
	ds_read_b128 v[198:201], v215
	ds_read_b128 v[202:205], v215 offset:2048
	ds_read_b128 v[206:209], v215 offset:4096
	ds_read_b128 v[210:213], v215 offset:6144
	s_waitcnt lgkmcnt(3)
	v_mfma_f32_16x16x32_bf16 v[152:155], v[198:201], v[164:167], v[152:155]
	v_mfma_f32_16x16x32_bf16 v[120:123], v[198:201], v[190:193], v[120:123]
	s_waitcnt lgkmcnt(2)
	v_mfma_f32_16x16x32_bf16 v[148:151], v[202:205], v[164:167], v[148:151]
	v_mfma_f32_16x16x32_bf16 v[96:99], v[202:205], v[190:193], v[96:99]
	s_waitcnt lgkmcnt(1)
	v_mfma_f32_16x16x32_bf16 v[144:147], v[206:209], v[164:167], v[144:147]
	v_mfma_f32_16x16x32_bf16 v[86:89], v[206:209], v[190:193], v[86:89]
	s_waitcnt lgkmcnt(0)
	v_mfma_f32_16x16x32_bf16 v[140:143], v[210:213], v[164:167], v[140:143]
	v_mfma_f32_16x16x32_bf16 v[82:85], v[210:213], v[190:193], v[82:85]
	ds_read_b128 v[198:201], v215 offset:8192
	ds_read_b128 v[202:205], v215 offset:10240
	ds_read_b128 v[206:209], v215 offset:12288
	ds_read_b128 v[210:213], v215 offset:14336
	s_waitcnt lgkmcnt(3)
	v_mfma_f32_16x16x32_bf16 v[136:139], v[198:201], v[164:167], v[136:139]
	v_mfma_f32_16x16x32_bf16 v[78:81], v[198:201], v[190:193], v[78:81]
	s_waitcnt lgkmcnt(2)
	v_mfma_f32_16x16x32_bf16 v[132:135], v[202:205], v[164:167], v[132:135]
	v_mfma_f32_16x16x32_bf16 v[74:77], v[202:205], v[190:193], v[74:77]
	s_waitcnt lgkmcnt(1)
	v_mfma_f32_16x16x32_bf16 v[128:131], v[206:209], v[164:167], v[128:131]
	v_mfma_f32_16x16x32_bf16 v[70:73], v[206:209], v[190:193], v[70:73]
	s_waitcnt lgkmcnt(0)
	v_mfma_f32_16x16x32_bf16 v[124:127], v[210:213], v[164:167], v[124:127]
	v_mfma_f32_16x16x32_bf16 v[66:69], v[210:213], v[190:193], v[66:69]
	v_add_u32_e32 v216, v173, v175
	ds_read_b128 v[164:167], v216 offset:32768
	ds_read_b128 v[190:193], v216 offset:34816
	v_add_u32_e32 v217, v176, v175
	ds_read_b128 v[198:201], v217
	ds_read_b128 v[202:205], v217 offset:2048
	ds_read_b128 v[206:209], v217 offset:4096
	ds_read_b128 v[210:213], v217 offset:6144
	s_waitcnt lgkmcnt(3)
	v_mfma_f32_16x16x32_bf16 v[152:155], v[198:201], v[164:167], v[152:155]
	v_mfma_f32_16x16x32_bf16 v[120:123], v[198:201], v[190:193], v[120:123]
	s_waitcnt lgkmcnt(2)
	v_mfma_f32_16x16x32_bf16 v[148:151], v[202:205], v[164:167], v[148:151]
	v_mfma_f32_16x16x32_bf16 v[96:99], v[202:205], v[190:193], v[96:99]
	s_waitcnt lgkmcnt(1)
	v_mfma_f32_16x16x32_bf16 v[144:147], v[206:209], v[164:167], v[144:147]
	v_mfma_f32_16x16x32_bf16 v[86:89], v[206:209], v[190:193], v[86:89]
	s_waitcnt lgkmcnt(0)
	v_mfma_f32_16x16x32_bf16 v[140:143], v[210:213], v[164:167], v[140:143]
	v_mfma_f32_16x16x32_bf16 v[82:85], v[210:213], v[190:193], v[82:85]
	ds_read_b128 v[198:201], v217 offset:8192
	ds_read_b128 v[202:205], v217 offset:10240
	ds_read_b128 v[206:209], v217 offset:12288
	ds_read_b128 v[210:213], v217 offset:14336
	s_min_u32 s33, s2, 5
	s_lshl_b32 s33, s33, 7
	s_waitcnt vmcnt(7)
	ds_write_b128 v189, v[104:107] offset:38912
	s_waitcnt vmcnt(6)
	ds_write_b128 v181, v[92:95] offset:39936
	s_waitcnt vmcnt(5)
	ds_write_b128 v189, v[112:115] offset:40960
	s_waitcnt vmcnt(4)
	ds_write_b128 v181, v[116:119] offset:41984
	s_addk_i32 s33, 0x100
	s_waitcnt lgkmcnt(7)
	v_mfma_f32_16x16x32_bf16 v[136:139], v[198:201], v[164:167], v[136:139]
	buffer_load_dwordx4 v[92:95], v182, s[4:7], s33 offen
	buffer_load_dwordx4 v[100:103], v183, s[4:7], s33 offen
	buffer_load_dwordx4 v[104:107], v184, s[4:7], s33 offen
	buffer_load_dwordx4 v[108:111], v185, s[4:7], s33 offen
	s_min_u32 s33, s2, 3
	s_waitcnt lgkmcnt(0)
	v_mfma_f32_16x16x32_bf16 v[132:135], v[202:205], v[164:167], v[132:135]
	s_barrier
; #define LAS __attribute__((address_space(3)))
; #define MS_WLOAD(set, t) do { _Pragma("unroll") for (int r_ = 0; r_ < 4; ++r_) wr[set][r_] = __builtin_bit_cast(f32x4, __builtin_amdgcn_raw_buffer_load_b128(wrs, (int)wvo + r_ * LDW * 4, MS_CL(t) * (64 * LDW * 4), 0)); } while (0)
; #define MS_WCOMMIT(set, bufi) do { LAS unsigned char* wb_ = lds + (bufi) * MS_TILE; _Pragma("unroll") for (int i_ = 0; i_ < 4; ++i_) { \
;             u32x2 p_; p_.x = pk2(wr[set][0][i_], wr[set][1][i_]); p_.y = pk2(wr[set][2][i_], wr[set][3][i_]); \
;             *(LAS u32x2*)(wb_ + ((i_ < 2) ? lw0 : lw1) + i_ * 128) = p_; } } while (0)
; #define MS_XSLOAD(t) do { _Pragma("unroll") for (int i_ = 0; i_ < 6; ++i_) xs[i_] = __builtin_bit_cast(bf16x8, __builtin_amdgcn_raw_buffer_load_b128(xrs, (int)xso[i_], MS_CL(t) * 128, 0)); } while (0)
; #define MS_XSWRITE(bufi) do { _Pragma("unroll") for (int i_ = 0; i_ < 6; ++i_) *(LAS bf16x8*)(xw + (bufi) * MS_XBUF + i_ * 1024 + ((i_ & 1) ? (xwo ^ 64) : xwo)) = xs[i_]; } while (0)
; #define MS_STEP(I, J, t) do { MS_WCOMMIT(J, J); MS_WLOAD(J, (t) + 3); MS_COMPUTE(I); MS_XSWRITE(J); MS_XSLOAD((t) + 2); __syncthreads(); } while (0)
;     ...
;             const LAS unsigned char* xr1 = lds + MS_XOFF + wave * MS_XWAVE + tk * 128 + (((4 + q) ^ rd_g) << 4);
;             __syncthreads();
;             MS_XSLOAD(0); MS_WLOAD(0, 0); MS_WLOAD(1, 1);
;             MS_WCOMMIT(0, 0); MS_WLOAD(0, 2);
;             MS_XSWRITE(0); MS_XSLOAD(1);
;             __syncthreads();
; #pragma unroll 1
;             for (int t = 0; t < NT; t += 2) { MS_STEP(0, 1, t); MS_STEP(1, 0, t + 1); }
	s_lshl_b32 s33, s33, 19
	v_mfma_f32_16x16x32_bf16 v[128:131], v[206:209], v[164:167], v[128:131]
	s_bitset1_b32 s33, 21
	v_mfma_f32_16x16x32_bf16 v[124:127], v[210:213], v[164:167], v[124:127]
	v_cvt_pk_bf16_f32 v164, v18, v22
	v_cvt_pk_bf16_f32 v165, v26, v30
	v_cvt_pk_bf16_f32 v18, v19, v23
	v_cvt_pk_bf16_f32 v19, v27, v31
	ds_write2_b64 v188, v[164:165], v[18:19] offset1:16
	v_cvt_pk_bf16_f32 v18, v20, v24
	v_cvt_pk_bf16_f32 v19, v28, v32
	v_cvt_pk_bf16_f32 v20, v21, v25
	v_cvt_pk_bf16_f32 v21, v29, v33
	ds_write2_b64 v180, v[18:19], v[20:21] offset0:32 offset1:48
	buffer_load_dwordx4 v[18:21], v160, s[8:11], s33 offen nt
	buffer_load_dwordx4 v[22:25], v90, s[8:11], s33 offen nt
	buffer_load_dwordx4 v[26:29], v178, s[8:11], s33 offen nt
	buffer_load_dwordx4 v[30:33], v179, s[8:11], s33 offen nt
	v_mfma_f32_16x16x32_bf16 v[78:81], v[198:201], v[190:193], v[78:81]
	v_mfma_f32_16x16x32_bf16 v[74:77], v[202:205], v[190:193], v[74:77]
	v_mfma_f32_16x16x32_bf16 v[70:73], v[206:209], v[190:193], v[70:73]
	v_mfma_f32_16x16x32_bf16 v[66:69], v[210:213], v[190:193], v[66:69]
	ds_read_b128 v[164:167], v214 offset:38912
	ds_read_b128 v[190:193], v214 offset:40960
	ds_read_b128 v[198:201], v215 offset:16384
	ds_read_b128 v[202:205], v215 offset:18432
	ds_read_b128 v[206:209], v215 offset:20480
	ds_read_b128 v[210:213], v215 offset:22528
	s_waitcnt lgkmcnt(3)
	v_mfma_f32_16x16x32_bf16 v[152:155], v[198:201], v[164:167], v[152:155]
	v_mfma_f32_16x16x32_bf16 v[120:123], v[198:201], v[190:193], v[120:123]
	s_waitcnt lgkmcnt(2)
	v_mfma_f32_16x16x32_bf16 v[148:151], v[202:205], v[164:167], v[148:151]
	v_mfma_f32_16x16x32_bf16 v[96:99], v[202:205], v[190:193], v[96:99]
	s_waitcnt lgkmcnt(1)
	v_mfma_f32_16x16x32_bf16 v[144:147], v[206:209], v[164:167], v[144:147]
	v_mfma_f32_16x16x32_bf16 v[86:89], v[206:209], v[190:193], v[86:89]
	s_waitcnt lgkmcnt(0)
	v_mfma_f32_16x16x32_bf16 v[140:143], v[210:213], v[164:167], v[140:143]
	v_mfma_f32_16x16x32_bf16 v[82:85], v[210:213], v[190:193], v[82:85]
	ds_read_b128 v[198:201], v215 offset:24576
	ds_read_b128 v[202:205], v215 offset:26624
	ds_read_b128 v[206:209], v215 offset:28672
	ds_read_b128 v[210:213], v215 offset:30720
	s_waitcnt lgkmcnt(3)
	v_mfma_f32_16x16x32_bf16 v[136:139], v[198:201], v[164:167], v[136:139]
	v_mfma_f32_16x16x32_bf16 v[78:81], v[198:201], v[190:193], v[78:81]
	s_waitcnt lgkmcnt(2)
	v_mfma_f32_16x16x32_bf16 v[132:135], v[202:205], v[164:167], v[132:135]
	v_mfma_f32_16x16x32_bf16 v[74:77], v[202:205], v[190:193], v[74:77]
	s_waitcnt lgkmcnt(1)
	v_mfma_f32_16x16x32_bf16 v[128:131], v[206:209], v[164:167], v[128:131]
	v_mfma_f32_16x16x32_bf16 v[70:73], v[206:209], v[190:193], v[70:73]
	s_waitcnt lgkmcnt(0)
	v_mfma_f32_16x16x32_bf16 v[124:127], v[210:213], v[164:167], v[124:127]
	v_mfma_f32_16x16x32_bf16 v[66:69], v[210:213], v[190:193], v[66:69]
	ds_read_b128 v[164:167], v216 offset:38912
	ds_read_b128 v[190:193], v216 offset:40960
	ds_read_b128 v[198:201], v217 offset:16384
	ds_read_b128 v[202:205], v217 offset:18432
	ds_read_b128 v[206:209], v217 offset:20480
	ds_read_b128 v[210:213], v217 offset:22528
	s_waitcnt lgkmcnt(3)
	v_mfma_f32_16x16x32_bf16 v[152:155], v[198:201], v[164:167], v[152:155]
	v_mfma_f32_16x16x32_bf16 v[120:123], v[198:201], v[190:193], v[120:123]
	s_waitcnt lgkmcnt(2)
	v_mfma_f32_16x16x32_bf16 v[148:151], v[202:205], v[164:167], v[148:151]
	v_mfma_f32_16x16x32_bf16 v[96:99], v[202:205], v[190:193], v[96:99]
	s_waitcnt lgkmcnt(1)
	v_mfma_f32_16x16x32_bf16 v[144:147], v[206:209], v[164:167], v[144:147]
	v_mfma_f32_16x16x32_bf16 v[86:89], v[206:209], v[190:193], v[86:89]
	s_waitcnt lgkmcnt(0)
	v_mfma_f32_16x16x32_bf16 v[140:143], v[210:213], v[164:167], v[140:143]
	v_mfma_f32_16x16x32_bf16 v[82:85], v[210:213], v[190:193], v[82:85]
	ds_read_b128 v[198:201], v217 offset:24576
	ds_read_b128 v[202:205], v217 offset:26624
	ds_read_b128 v[206:209], v217 offset:28672
	ds_read_b128 v[210:213], v217 offset:30720
	s_lshl_b32 s3, s3, 7
	s_waitcnt vmcnt(7)
	ds_write_b128 v189, v[92:95] offset:32768
	s_waitcnt vmcnt(6)
	ds_write_b128 v181, v[100:103] offset:33792
	s_waitcnt vmcnt(5)
	ds_write_b128 v189, v[104:107] offset:34816
	s_waitcnt vmcnt(4)
	ds_write_b128 v181, v[108:111] offset:35840
	s_addk_i32 s3, 0x180
	buffer_load_dwordx4 v[104:107], v182, s[4:7], s3 offen
	buffer_load_dwordx4 v[92:95], v183, s[4:7], s3 offen
	buffer_load_dwordx4 v[112:115], v184, s[4:7], s3 offen
	buffer_load_dwordx4 v[116:119], v185, s[4:7], s3 offen
	s_waitcnt lgkmcnt(7)
	v_mfma_f32_16x16x32_bf16 v[136:139], v[198:201], v[164:167], v[136:139]
	s_cmp_gt_u32 s2, 5
	s_waitcnt lgkmcnt(0)
	s_barrier
	v_mfma_f32_16x16x32_bf16 v[78:81], v[198:201], v[190:193], v[78:81]
	v_mfma_f32_16x16x32_bf16 v[132:135], v[202:205], v[164:167], v[132:135]
	v_mfma_f32_16x16x32_bf16 v[74:77], v[202:205], v[190:193], v[74:77]
	v_mfma_f32_16x16x32_bf16 v[128:131], v[206:209], v[164:167], v[128:131]
	v_mfma_f32_16x16x32_bf16 v[70:73], v[206:209], v[190:193], v[70:73]
	v_mfma_f32_16x16x32_bf16 v[124:127], v[210:213], v[164:167], v[124:127]
	v_mfma_f32_16x16x32_bf16 v[66:69], v[210:213], v[190:193], v[66:69]
	s_cbranch_scc0 .Lmoe_l_b
